# rider split 8 tiles in the GQA units / 16 in the differential units
# speedup vs baseline: 1.0153x; 1.0153x over previous
; DI f32x16 mfma8(v8i a, v8i b, f32x16 c) { return __builtin_amdgcn_mfma_scale_f32_32x32x64_f8f6f4(a, b, c, 0, 0, 0, 0, 0, 0); }
; DI void attn_unit_d8(unsigned char* lds, const AttnArgs& a) {
;     ...
;     auto tile = [&](const unsigned char* Kb, const unsigned char* Kn, v8i& Pa, v8i& Pb, v8i& v0, v8i& v1, const v8i& Qa, const v8i& Qb, const v8i& w0, const v8i& w1) __attribute__((always_inline)) {
;         qk(Kb, 1, s1a, s1b);
;         v0 = rd32(Kb + voff); v1 = rd32(Kb + voff + 32 * A8_PITCH);
;         o0[0] = mfma8(w0, Qa, o0[0]); o1[0] = mfma8(w0, Qb, o1[0]); o0[1] = mfma8(w1, Qa, o0[1]); o1[1] = mfma8(w1, Qb, o1[1]);
;         expsum(s0a, l0); expsum(s0b, l1); pack4(s0a, Pa, 0); pack4(s0b, Pb, 0);
;         qk(Kn, 0, s0a, s0b);
;         expsum(s1a, l0); expsum(s1b, l1); pack4(s1a, Pa, 4); pack4(s1b, Pb, 4);
; #pragma unroll
;         for (int i = 0; i < 8; ++i) { __builtin_amdgcn_sched_group_barrier(0x008, 1, 0); __builtin_amdgcn_sched_group_barrier(0x402, 22, 0); }
;     };
;     for (int t = a.t0; t < a.t1; t += 2) {
;         const int s1 = sb + 1 >= 5 ? sb - 4 : sb + 1, s2 = sb + 2 >= 5 ? sb - 3 : sb + 2, s3 = sb + 3 >= 5 ? sb - 2 : sb + 3, s4 = sb + 4 >= 5 ? sb - 1 : sb + 4;
;         { const int ta = t + 3, tb = t + 4; gload(ta < a.t1 ? ta : a.t1 - 1, kreg0, vreg0); gload(tb < a.t1 ? tb : a.t1 - 1, kreg1, vreg1); }
;         tile(lds + sb * D8_SLOT, lds + s1 * D8_SLOT, PaX, PbX, vX0, vX1, PaY, PbY, vY0, vY1);
;         tile(lds + s1 * D8_SLOT, lds + s2 * D8_SLOT, PaY, PbY, vY0, vY1, PaX, PbX, vX0, vX1);
.LBB0_663:
	s_cmp_gt_i32 s16, 3
	s_cselect_b32 s17, -4, 1
	s_add_i32 s18, s17, s16
	s_mul_i32 s6, s16, 0x2800
	s_cmp_gt_i32 s16, 2
	v_mfma_f32_32x32x64_f8f6f4 v[50:65], v[154:161], v[138:145], v[50:65]
	v_exp_f32_e32 v192, v90
	v_add_u32_e32 v90, s6, v218
	s_cselect_b32 s6, -3, 2
	s_add_i32 s6, s6, s16
	s_cmp_gt_i32 s16, 1
	s_cselect_b32 s19, -2, 3
	s_add_i32 s19, s19, s16
	s_cmp_gt_i32 s16, 0
	s_cselect_b32 s49, -1, 4
	s_min_u32 s54, s46, 64
	s_add_i32 s49, s49, s16
	s_cmp_lt_u32 s46, 61
	s_mul_i32 s17, s6, 0x2800
	s_mov_b32 s16, s6
	s_cselect_b64 s[52:53], -1, 0
	s_lshl_b32 s6, s54, 6
	s_add_i32 s54, s6, 0xc0
	s_add_i32 s55, s6, 0xfffff0c0
	s_and_b64 s[52:53], s[52:53], exec
	v_lshl_add_u64 v[98:99], v[182:183], 0, s[6:7]
	s_cselect_b32 s6, s54, s55
	s_cselect_b32 s53, s21, s48
	s_cselect_b32 s52, s20, s47
	s_min_u32 s56, s46, 63
	v_exp_f32_e32 v198, v82
	v_exp_f32_e32 v199, v83
	v_exp_f32_e32 v196, v84
	v_exp_f32_e32 v197, v85
	v_exp_f32_e32 v200, v86
	v_exp_f32_e32 v201, v87
	v_exp_f32_e32 v194, v88
	v_exp_f32_e32 v195, v89
	ds_read_b128 v[82:85], v90 offset:2560
	ds_read_b128 v[86:89], v90 offset:2576
	global_load_dwordx2 v[202:203], v[98:99], off offset:192
	v_add_u32_e32 v98, s6, v215
	s_cmp_lt_u32 s46, 60
	v_ashrrev_i32_e32 v99, 31, v98
	s_cselect_b64 s[54:55], -1, 0
	s_lshl_b32 s6, s56, 6
	v_lshlrev_b64 v[98:99], 8, v[98:99]
	s_add_i32 s56, s6, 0x100
	s_add_i32 s57, s6, 0xfffff100
	v_lshl_add_u64 v[98:99], s[52:53], 0, v[98:99]
	s_and_b64 s[52:53], s[54:55], exec
	s_cselect_b32 s54, s56, s57
	v_lshl_add_u64 v[220:221], v[98:99], 0, v[178:179]
	v_add_u32_e32 v98, s54, v215
	v_ashrrev_i32_e32 v99, 31, v98
	s_cselect_b32 s53, s21, s48
	s_cselect_b32 s52, s20, s47
	v_lshlrev_b64 v[98:99], 8, v[98:99]
	v_lshl_add_u64 v[100:101], v[182:183], 0, s[6:7]
	v_lshl_add_u64 v[98:99], s[52:53], 0, v[98:99]
	global_load_dwordx2 v[204:205], v[100:101], off offset:256
	v_lshl_add_u64 v[222:223], v[98:99], 0, v[178:179]
	s_waitcnt lgkmcnt(0)
	v_mfma_f32_32x32x64_f8f6f4 v[98:113], v[82:89], v[114:121], 0
	v_exp_f32_e32 v193, v91
	v_exp_f32_e32 v224, v92
	v_exp_f32_e32 v225, v93
	v_exp_f32_e32 v226, v94
	v_exp_f32_e32 v227, v95
	v_exp_f32_e32 v228, v96
	v_exp_f32_e32 v229, v97
	ds_read_b128 v[170:173], v90 offset:5120
	ds_read_b128 v[174:177], v90 offset:5136
	ds_read_b128 v[162:165], v90 offset:7680
	ds_read_b128 v[166:169], v90 offset:7696
	v_pk_add_f32 v[90:91], v[186:187], v[198:199]
	v_pk_add_f32 v[92:93], v[184:185], v[196:197]
	v_pk_add_f32 v[90:91], v[200:201], v[90:91]
	v_pk_add_f32 v[92:93], v[194:195], v[92:93]
	v_pk_add_f32 v[90:91], v[192:193], v[90:91]
	v_pk_add_f32 v[92:93], v[224:225], v[92:93]
	v_exp_f32_e32 v66, v66
	v_exp_f32_e32 v67, v67
	v_exp_f32_e32 v68, v68
	v_exp_f32_e32 v69, v69
	v_exp_f32_e32 v70, v70
	v_exp_f32_e32 v71, v71
	v_exp_f32_e32 v72, v72
	v_pk_add_f32 v[230:231], v[228:229], v[92:93]
	v_pk_add_f32 v[232:233], v[226:227], v[90:91]
	v_mfma_f32_32x32x64_f8f6f4 v[82:97], v[82:89], v[122:129], 0
	v_exp_f32_e32 v73, v73
	v_exp_f32_e32 v74, v74
	v_exp_f32_e32 v75, v75
	v_exp_f32_e32 v76, v76
	v_exp_f32_e32 v77, v77
	v_exp_f32_e32 v78, v78
	v_exp_f32_e32 v79, v79
	v_exp_f32_e32 v80, v80
	v_exp_f32_e32 v81, v81
	v_pk_add_f32 v[186:187], v[190:191], v[66:67]
	v_pk_add_f32 v[188:189], v[188:189], v[68:69]
	s_nop 0
	v_pk_add_f32 v[186:187], v[70:71], v[186:187]
	v_pk_add_f32 v[188:189], v[72:73], v[188:189]
	s_nop 0
	v_cvt_scalef32_pk_fp8_f32 v184, v198, v199, s36
	v_pk_add_f32 v[186:187], v[74:75], v[186:187]
	v_pk_add_f32 v[188:189], v[76:77], v[188:189]
	v_cvt_scalef32_pk_fp8_f32 v185, v200, v201, s36
	v_cvt_scalef32_pk_fp8_f32 v184, v196, v197, s36 op_sel:[0,0,0,1]
	v_pk_add_f32 v[190:191], v[78:79], v[186:187]
	v_pk_add_f32 v[188:189], v[80:81], v[188:189]
	v_mfma_f32_32x32x64_f8f6f4 v[2:17], v[154:161], v[130:137], v[2:17]
	s_nop 0
	s_nop 0
	s_nop 0
	s_nop 0
	s_nop 0
	s_nop 0
	s_mulk_i32 s18, 0x2800
	v_cvt_scalef32_pk_fp8_f32 v186, v192, v193, s36
	v_cvt_scalef32_pk_fp8_f32 v187, v226, v227, s36
	v_cvt_scalef32_pk_fp8_f32 v154, v66, v67, s36
	v_cvt_scalef32_pk_fp8_f32 v155, v70, v71, s36
	v_cvt_scalef32_pk_fp8_f32 v156, v74, v75, s36
	v_cvt_scalef32_pk_fp8_f32 v157, v78, v79, s36
	v_cvt_scalef32_pk_fp8_f32 v185, v194, v195, s36 op_sel:[0,0,0,1]
	v_add_u32_e32 v219, s18, v218
	v_cvt_scalef32_pk_fp8_f32 v186, v224, v225, s36 op_sel:[0,0,0,1]
	v_cvt_scalef32_pk_fp8_f32 v187, v228, v229, s36 op_sel:[0,0,0,1]
	v_cvt_scalef32_pk_fp8_f32 v154, v68, v69, s36 op_sel:[0,0,0,1]
	v_cvt_scalef32_pk_fp8_f32 v155, v72, v73, s36 op_sel:[0,0,0,1]
	v_cvt_scalef32_pk_fp8_f32 v156, v76, v77, s36 op_sel:[0,0,0,1]
	v_cvt_scalef32_pk_fp8_f32 v157, v80, v81, s36 op_sel:[0,0,0,1]
	v_exp_f32_e32 v98, v98
	v_exp_f32_e32 v99, v99
	v_mfma_f32_32x32x64_f8f6f4 v[34:49], v[146:153], v[138:145], v[34:49]
	v_exp_f32_e32 v100, v100
	v_exp_f32_e32 v101, v101
	v_exp_f32_e32 v102, v102
	v_exp_f32_e32 v103, v103
	v_exp_f32_e32 v104, v104
	v_exp_f32_e32 v105, v105
	v_exp_f32_e32 v106, v106
	v_exp_f32_e32 v107, v107
	v_exp_f32_e32 v108, v108
	v_exp_f32_e32 v109, v109
	v_exp_f32_e32 v110, v110
	v_exp_f32_e32 v111, v111
	v_exp_f32_e32 v112, v112
	v_exp_f32_e32 v113, v113
	ds_read_b128 v[192:195], v219
	ds_read_b128 v[196:199], v219 offset:16
	v_pk_add_f32 v[66:67], v[232:233], v[98:99]
	v_pk_add_f32 v[68:69], v[230:231], v[100:101]
	v_pk_add_f32 v[66:67], v[102:103], v[66:67]
	v_pk_add_f32 v[68:69], v[104:105], v[68:69]
	v_pk_add_f32 v[66:67], v[106:107], v[66:67]
	v_pk_add_f32 v[68:69], v[108:109], v[68:69]
	v_pk_add_f32 v[140:141], v[110:111], v[66:67]
	v_pk_add_f32 v[138:139], v[112:113], v[68:69]
	v_mfma_f32_32x32x64_f8f6f4 v[18:33], v[146:153], v[130:137], v[18:33]
	v_exp_f32_e32 v82, v82
	v_exp_f32_e32 v83, v83
	v_exp_f32_e32 v84, v84
	v_exp_f32_e32 v85, v85
	v_exp_f32_e32 v86, v86
	v_exp_f32_e32 v87, v87
	v_exp_f32_e32 v88, v88
	v_exp_f32_e32 v89, v89
	v_exp_f32_e32 v90, v90
	v_exp_f32_e32 v91, v91
	v_exp_f32_e32 v92, v92
	v_exp_f32_e32 v93, v93
	v_exp_f32_e32 v94, v94
	v_exp_f32_e32 v95, v95
	v_exp_f32_e32 v96, v96
	v_exp_f32_e32 v97, v97
	v_pk_add_f32 v[66:67], v[190:191], v[82:83]
	v_pk_add_f32 v[68:69], v[188:189], v[84:85]
	v_pk_add_f32 v[66:67], v[86:87], v[66:67]
	v_pk_add_f32 v[68:69], v[88:89], v[68:69]
	v_pk_add_f32 v[130:131], v[90:91], v[66:67]
	v_pk_add_f32 v[132:133], v[92:93], v[68:69]
	s_waitcnt lgkmcnt(0)
; DI KParamsPtr kparams() { KParamsPtr p = (KParamsPtr)__builtin_amdgcn_kernarg_segment_ptr(); asm volatile("" : "+s"(p)); return p; }
; DI f32x16 mfma8(v8i a, v8i b, f32x16 c) { return __builtin_amdgcn_mfma_scale_f32_32x32x64_f8f6f4(a, b, c, 0, 0, 0, 0, 0, 0); }
; DI void attn_unit_a8(unsigned char* lds, const AttnArgs& a) {
;     ...
;     auto w_decode = [&](int j, const float*& src, unsigned char*& dst, int& ld, int& n0, int& k0, bool& gu) __attribute__((always_inline)) {
;         const int g = (j >> 2) * 512 + a.wl, e = g / 96, rr = g - e * 96; KParamsPtr kp = kparams();
;         if (rr < 64) { src = kp->w_gu + ((size_t)a.wli * NE + e) * (1024 * 2048); dst = kp->ws + WS_WGU + (size_t)a.wli * SZ_WGU + (size_t)e * 2048 * 1024; ld = 2048; n0 = (rr & 7) * 256; k0 = ((rr >> 3) * 4 + (j & 3)) * 32; gu = true; }
;         else { const int q = rr - 64; src = kp->w_dn + ((size_t)a.wli * NE + e) * (1024 * 1024); dst = kp->ws + WS_WDN + (size_t)a.wli * SZ_WDN + (size_t)e * 1024 * 1024; ld = 1024; n0 = (q & 3) * 256; k0 = ((q >> 2) * 4 + (j & 3)) * 32; gu = false; } };
; DI void attn_unit_d8(unsigned char* lds, const AttnArgs& a) {
;     ...
;     auto tile = [&](const unsigned char* Kb, const unsigned char* Kn, v8i& Pa, v8i& Pb, v8i& v0, v8i& v1, const v8i& Qa, const v8i& Qb, const v8i& w0, const v8i& w1) __attribute__((always_inline)) {
;         qk(Kb, 1, s1a, s1b);
;         v0 = rd32(Kb + voff); v1 = rd32(Kb + voff + 32 * A8_PITCH);
;         o0[0] = mfma8(w0, Qa, o0[0]); o1[0] = mfma8(w0, Qb, o1[0]); o0[1] = mfma8(w1, Qa, o0[1]); o1[1] = mfma8(w1, Qb, o1[1]);
;         expsum(s0a, l0); expsum(s0b, l1); pack4(s0a, Pa, 0); pack4(s0b, Pb, 0);
;         qk(Kn, 0, s0a, s0b);
;         expsum(s1a, l0); expsum(s1b, l1); pack4(s1a, Pa, 4); pack4(s1b, Pb, 4);
; #pragma unroll
;         for (int i = 0; i < 8; ++i) { __builtin_amdgcn_sched_group_barrier(0x008, 1, 0); __builtin_amdgcn_sched_group_barrier(0x402, 22, 0); }
;     };
	v_mfma_f32_32x32x64_f8f6f4 v[66:81], v[192:199], v[114:121], 0
	s_nop 0
	s_nop 0
	s_nop 0
	s_nop 0
	s_nop 0
	s_nop 0
	s_nop 0
	v_cvt_scalef32_pk_fp8_f32 v188, v98, v99, s36
	v_cvt_scalef32_pk_fp8_f32 v189, v102, v103, s36
	v_cvt_scalef32_pk_fp8_f32 v190, v106, v107, s36
	v_cvt_scalef32_pk_fp8_f32 v191, v110, v111, s36
	v_cvt_scalef32_pk_fp8_f32 v158, v82, v83, s36
	v_cvt_scalef32_pk_fp8_f32 v159, v86, v87, s36
	v_pk_add_f32 v[142:143], v[96:97], v[132:133]
	v_pk_add_f32 v[144:145], v[94:95], v[130:131]
	v_cvt_scalef32_pk_fp8_f32 v160, v90, v91, s36
	v_cvt_scalef32_pk_fp8_f32 v188, v100, v101, s36 op_sel:[0,0,0,1]
	v_cvt_scalef32_pk_fp8_f32 v189, v104, v105, s36 op_sel:[0,0,0,1]
	v_cvt_scalef32_pk_fp8_f32 v190, v108, v109, s36 op_sel:[0,0,0,1]
	v_cvt_scalef32_pk_fp8_f32 v191, v112, v113, s36 op_sel:[0,0,0,1]
	v_cvt_scalef32_pk_fp8_f32 v158, v84, v85, s36 op_sel:[0,0,0,1]
	v_cvt_scalef32_pk_fp8_f32 v159, v88, v89, s36 op_sel:[0,0,0,1]
	v_mfma_f32_32x32x64_f8f6f4 v[98:113], v[192:199], v[122:129], 0
	global_load_dwordx2 v[192:193], v[220:221], off
	global_load_dwordx2 v[194:195], v[222:223], off
	ds_read_b128 v[130:133], v219 offset:2560
	ds_read_b128 v[134:137], v219 offset:2576
	s_mulk_i32 s19, 0x2800
	s_nop 0
	v_exp_f32_e32 v146, v66
	s_lshr_b32 s73, s61, 2
	v_exp_f32_e32 v147, v67
	s_add_i32 s73, s73, 2
	v_exp_f32_e32 v148, v68
	s_lshl_b32 s73, s73, 9
	v_exp_f32_e32 v149, v69
	s_add_i32 s73, s73, s42
	s_add_i32 s19, s19, 0
	v_cvt_scalef32_pk_fp8_f32 v161, v94, v95, s36
	v_exp_f32_e32 v150, v70
	s_mul_i32 s75, s73, 0xaaab
	v_exp_f32_e32 v151, v71
	s_lshr_b32 s75, s75, 22
	v_exp_f32_e32 v152, v72
	s_mul_i32 s76, s75, 0x60
	v_exp_f32_e32 v153, v73
	s_sub_i32 s76, s73, s76
	v_add_u32_e32 v224, s19, v216
	v_add_u32_e32 v225, s19, v217
	v_cvt_scalef32_pk_fp8_f32 v160, v92, v93, s36 op_sel:[0,0,0,1]
	v_cvt_scalef32_pk_fp8_f32 v161, v96, v97, s36 op_sel:[0,0,0,1]
	v_exp_f32_e32 v196, v74
	s_lshr_b32 s77, s76, 6
	v_exp_f32_e32 v197, v75
	s_lshl_b32 s78, s77, 6
	v_exp_f32_e32 v198, v76
	s_sub_i32 s76, s76, s78
	v_exp_f32_e32 v199, v77
	s_sub_i32 s78, 3, s77
	v_exp_f32_e32 v200, v78
	s_lshr_b32 s79, s76, s78
	v_exp_f32_e32 v201, v79
	s_lshl_b32 s79, s79, 2
	v_exp_f32_e32 v220, v80
	s_and_b32 s81, s61, 3
	v_exp_f32_e32 v221, v81
	s_add_i32 s79, s79, s81
	s_waitcnt lgkmcnt(0)
	v_mfma_f32_32x32x64_f8f6f4 v[82:97], v[130:137], v[114:121], 0
	v_add_f32_e64 v66, v140, v146
	v_add_f32_e64 v67, v141, v147
	v_add_f32_e64 v68, v138, v148
	v_add_f32_e64 v69, v139, v149
	v_add_f32_e64 v66, v150, v66
	v_add_f32_e64 v67, v151, v67
	v_add_f32_e64 v68, v152, v68
	v_add_f32_e64 v69, v153, v69
	v_add_f32_e64 v138, v196, v66
	v_add_f32_e64 v139, v197, v67
	v_add_f32_e64 v140, v198, v68
	v_add_f32_e64 v141, v199, v69
	v_exp_f32_e32 v98, v98
	s_lshl_b32 s79, s79, 5
	v_exp_f32_e32 v99, v99
	s_lshl_b32 s81, s63, 2
	v_exp_f32_e32 v100, v100
	s_add_i32 s81, s81, s79
	v_exp_f32_e32 v101, v101
	s_sub_i32 s78, 13, s77
	v_exp_f32_e32 v102, v102
	s_lshl_b32 s81, s81, s78
	v_exp_f32_e32 v103, v103
	s_lshr_b32 s78, 7, s77
	v_exp_f32_e32 v104, v104
	s_and_b32 s78, s76, s78
	v_exp_f32_e32 v105, v105
	s_lshl_b32 s72, s78, 10
	v_exp_f32_e32 v106, v106
	s_add_i32 s81, s81, s72
	v_exp_f32_e32 v107, v107
	s_add_i32 s72, s75, 0
	v_exp_f32_e32 v108, v108
	s_sub_i32 s80, 23, s77
	v_exp_f32_e32 v109, v109
	s_lshl_b32 s72, s72, s80
	v_exp_f32_e32 v110, v110
	s_add_i32 s81, s81, s72
	v_exp_f32_e32 v111, v111
	s_cmp_eq_u32 s77, 0
	s_cselect_b64 s[84:85], s[66:67], s[68:69]
	v_exp_f32_e32 v112, v112
	s_add_u32 s84, s84, s81
	s_addc_u32 s85, s85, 0
	v_exp_f32_e32 v113, v113
	s_lshr_b32 s80, 0x2000, s77
	v_mfma_f32_32x32x64_f8f6f4 v[66:81], v[130:137], v[122:129], 0
	v_add_f32_e64 v130, v144, v98
	v_add_f32_e64 v131, v145, v99
	v_add_f32_e64 v132, v142, v100
	v_add_f32_e64 v133, v143, v101
	v_add_f32_e64 v142, v102, v130
	v_add_f32_e64 v143, v103, v131
	v_add_f32_e64 v132, v104, v132
	v_add_f32_e64 v133, v105, v133
	v_add_f32_e64 v134, v220, v140
	v_add_f32_e64 v135, v221, v141
	v_add_f32_e64 v136, v200, v138
	v_add_f32_e64 v137, v201, v139
	s_nop 0
	s_nop 0
	s_nop 0
	s_nop 0
	s_nop 0
	s_nop 0
	v_pk_add_f32 v[142:143], v[106:107], v[142:143]
	v_pk_add_f32 v[132:133], v[108:109], v[132:133]
	v_cvt_scalef32_pk_fp8_f32 v138, v146, v147, s36
	v_cvt_scalef32_pk_fp8_f32 v139, v150, v151, s36
	v_cvt_scalef32_pk_fp8_f32 v140, v196, v197, s36
	v_cvt_scalef32_pk_fp8_f32 v141, v200, v201, s36
	v_cvt_scalef32_pk_fp8_f32 v130, v98, v99, s36
	v_cvt_scalef32_pk_fp8_f32 v131, v102, v103, s36
	v_pk_add_f32 v[146:147], v[112:113], v[132:133]
	v_pk_add_f32 v[150:151], v[110:111], v[142:143]
	v_mfma_f32_32x32x64_f8f6f4 v[50:65], v[170:177], v[184:191], v[50:65]
	v_exp_f32_e32 v82, v82
	s_and_b32 s72, s78, 3
	v_exp_f32_e32 v83, v83
	s_lshl_b32 s72, s72, 19
	v_exp_f32_e32 v84, v84
	s_lshr_b32 s81, s78, 2
	v_exp_f32_e32 v85, v85
	s_lshl_b32 s81, s81, 17
	v_add_u32_e32 v102, s17, v218
	v_exp_f32_e32 v86, v86
	s_add_i32 s72, s72, s81
	v_exp_f32_e32 v87, v87
	s_lshl_b32 s81, s78, 18
	v_exp_f32_e32 v88, v88
	s_cmp_eq_u32 s77, 0
	s_cselect_b32 s72, s72, s81
; DI void attn_unit_a8(unsigned char* lds, const AttnArgs& a) {
;     ...
;     auto w_cvt = [&]() __attribute__((always_inline)) { unsigned char* t8 = lds + AT_WT + wn4 * WPITCH + 4 * wid;
; #pragma unroll
;         for (int j = 0; j < 4; ++j) *(unsigned*)(t8 + j * WPITCH) = pk4_fp8_mul64(wq[0][j], wq[1][j], wq[2][j], wq[3][j]); };
;     const int wcol = tid >> 1, whalf = tid & 1;
;     const unsigned wper_gu = (unsigned)((wcol >> 7) * 256 + (wcol & 96) + invperm32(wcol & 31)) * 1024u + 16u * whalf;
;     const unsigned wper_dn = (unsigned)fwd_lane16(wcol) * 1024u + 16u * whalf;
;     auto w_store = [&](int j) __attribute__((always_inline)) { const float* src; unsigned char* dst; int ld, n0, k0; bool gu; w_decode(j, src, dst, ld, n0, k0, gu);
;         const int nb = n0 >> 8; const unsigned uni = (unsigned)(gu ? (nb & 3) * 512 + (nb >> 2) * 128 : nb * 256) * 1024u + (unsigned)k0;
; DI void attn_unit_d8(unsigned char* lds, const AttnArgs& a) {
;     ...
;     auto tile = [&](const unsigned char* Kb, const unsigned char* Kn, v8i& Pa, v8i& Pb, v8i& v0, v8i& v1, const v8i& Qa, const v8i& Qb, const v8i& w0, const v8i& w1) __attribute__((always_inline)) {
;         qk(Kb, 1, s1a, s1b);
;         v0 = rd32(Kb + voff); v1 = rd32(Kb + voff + 32 * A8_PITCH);
;         o0[0] = mfma8(w0, Qa, o0[0]); o1[0] = mfma8(w0, Qb, o1[0]); o0[1] = mfma8(w1, Qa, o0[1]); o1[1] = mfma8(w1, Qb, o1[1]);
;         expsum(s0a, l0); expsum(s0b, l1); pack4(s0a, Pa, 0); pack4(s0b, Pb, 0);
;         qk(Kn, 0, s0a, s0b);
;         expsum(s1a, l0); expsum(s1b, l1); pack4(s1a, Pa, 4); pack4(s1b, Pb, 4);
; #pragma unroll
;         for (int i = 0; i < 8; ++i) { __builtin_amdgcn_sched_group_barrier(0x008, 1, 0); __builtin_amdgcn_sched_group_barrier(0x402, 22, 0); }
;     };
;     for (int t = a.t0; t < a.t1; t += 2) {
;         const int s1 = sb + 1 >= 5 ? sb - 4 : sb + 1, s2 = sb + 2 >= 5 ? sb - 3 : sb + 2, s3 = sb + 3 >= 5 ? sb - 2 : sb + 3, s4 = sb + 4 >= 5 ? sb - 1 : sb + 4;
;         { const int ta = t + 3, tb = t + 4; gload(ta < a.t1 ? ta : a.t1 - 1, kreg0, vreg0); gload(tb < a.t1 ? tb : a.t1 - 1, kreg1, vreg1); }
;         tile(lds + sb * D8_SLOT, lds + s1 * D8_SLOT, PaX, PbX, vX0, vX1, PaY, PbY, vY0, vY1);
;         tile(lds + s1 * D8_SLOT, lds + s2 * D8_SLOT, PaY, PbY, vY0, vY1, PaX, PbX, vX0, vX1);
;         lstore(s3, kreg0, vreg0); lstore(s4, kreg1, vreg1);
	v_exp_f32_e32 v89, v89
	s_mul_i32 s81, s77, 0x10000000
	v_cvt_scalef32_pk_fp8_f32 v130, v100, v101, s36 op_sel:[0,0,0,1]
	v_cvt_scalef32_pk_fp8_f32 v131, v104, v105, s36 op_sel:[0,0,0,1]
	v_exp_f32_e32 v90, v90
	s_add_i32 s81, s81, 0x1094000
	v_exp_f32_e32 v91, v91
	s_add_i32 s72, s72, s79
	v_exp_f32_e32 v92, v92
	s_sub_i32 s73, 21, s77
	v_exp_f32_e32 v93, v93
	s_lshl_b32 s73, s75, s73
	ds_read_b128 v[98:101], v102
	ds_read_b128 v[102:105], v102 offset:16
	s_nop 0
	v_cvt_scalef32_pk_fp8_f32 v138, v148, v149, s36 op_sel:[0,0,0,1]
	v_cvt_scalef32_pk_fp8_f32 v139, v152, v153, s36 op_sel:[0,0,0,1]
	v_cvt_scalef32_pk_fp8_f32 v140, v198, v199, s36 op_sel:[0,0,0,1]
	v_cvt_scalef32_pk_fp8_f32 v141, v220, v221, s36 op_sel:[0,0,0,1]
	s_nop 0
	v_exp_f32_e32 v94, v94
	s_add_i32 s72, s72, s73
	v_mfma_f32_32x32x64_f8f6f4 v[2:17], v[170:177], v[154:161], v[2:17]
	v_exp_f32_e32 v148, v96
	s_add_u32 s72, s72, s81
	v_cvt_scalef32_pk_fp8_f32 v132, v106, v107, s36
	v_exp_f32_e32 v149, v97
	s_or_b32 s79, s72, s77
	v_pk_add_f32 v[96:97], v[136:137], v[82:83]
	v_pk_add_f32 v[106:107], v[134:135], v[84:85]
	v_exp_f32_e32 v66, v66
	v_exp_f32_e32 v67, v67
	v_exp_f32_e32 v68, v68
	v_exp_f32_e32 v69, v69
	v_exp_f32_e32 v95, v95
	v_cvt_scalef32_pk_fp8_f32 v133, v110, v111, s36
	v_pk_add_f32 v[106:107], v[88:89], v[106:107]
	v_pk_add_f32 v[96:97], v[86:87], v[96:97]
	v_exp_f32_e32 v70, v70
	v_exp_f32_e32 v71, v71
	v_exp_f32_e32 v72, v72
	v_exp_f32_e32 v73, v73
	v_cvt_scalef32_pk_fp8_f32 v132, v108, v109, s36 op_sel:[0,0,0,1]
	v_cvt_scalef32_pk_fp8_f32 v133, v112, v113, s36 op_sel:[0,0,0,1]
	v_pk_add_f32 v[96:97], v[90:91], v[96:97]
	v_pk_add_f32 v[106:107], v[92:93], v[106:107]
	v_exp_f32_e32 v74, v74
	v_mfma_f32_32x32x64_f8f6f4 v[34:49], v[162:169], v[184:191], v[34:49]
	v_exp_f32_e32 v75, v75
	v_exp_f32_e32 v76, v76
	v_exp_f32_e32 v77, v77
	v_exp_f32_e32 v78, v78
	v_exp_f32_e32 v79, v79
	s_nop 0
	v_exp_f32_e32 v80, v80
	v_exp_f32_e32 v81, v81
	s_nop 0
	s_nop 0
	v_cvt_scalef32_pk_fp8_f32 v142, v82, v83, s36
	s_nop 0
	v_cvt_scalef32_pk_fp8_f32 v143, v86, v87, s36
	v_cvt_scalef32_pk_fp8_f32 v144, v90, v91, s36
	v_cvt_scalef32_pk_fp8_f32 v142, v84, v85, s36 op_sel:[0,0,0,1]
	v_pk_add_f32 v[82:83], v[150:151], v[66:67]
	v_pk_add_f32 v[84:85], v[146:147], v[68:69]
	s_mulk_i32 s49, 0x2800
	v_pk_add_f32 v[184:185], v[148:149], v[106:107]
	v_pk_add_f32 v[186:187], v[94:95], v[96:97]
	v_cvt_scalef32_pk_fp8_f32 v145, v94, v95, s36
	v_cvt_scalef32_pk_fp8_f32 v143, v88, v89, s36 op_sel:[0,0,0,1]
	v_cvt_scalef32_pk_fp8_f32 v144, v92, v93, s36 op_sel:[0,0,0,1]
	v_mfma_f32_32x32x64_f8f6f4 v[18:33], v[162:169], v[154:161], v[18:33]
	v_add_f32_e64 v84, v72, v84
	v_add_f32_e64 v85, v73, v85
	v_add_f32_e64 v82, v70, v82
	v_add_f32_e64 v83, v71, v83
	s_nop 0
	s_nop 0
	s_nop 0
	s_nop 0
	s_add_i32 s6, s49, 0
	v_add_f32_e64 v82, v74, v82
	v_add_f32_e64 v83, v75, v83
	v_add_f32_e64 v84, v76, v84
	v_add_f32_e64 v85, v77, v85
	v_cvt_scalef32_pk_fp8_f32 v134, v66, v67, s36
	v_cvt_scalef32_pk_fp8_f32 v135, v70, v71, s36
	v_cvt_scalef32_pk_fp8_f32 v136, v74, v75, s36
	v_cvt_scalef32_pk_fp8_f32 v137, v78, v79, s36
	v_pk_add_f32 v[188:189], v[80:81], v[84:85]
	v_pk_add_f32 v[190:191], v[78:79], v[82:83]
	v_add_u32_e32 v106, s6, v216
	v_add_u32_e32 v107, s6, v217
	v_cvt_scalef32_pk_fp8_f32 v145, v148, v149, s36 op_sel:[0,0,0,1]
	v_cvt_scalef32_pk_fp8_f32 v134, v68, v69, s36 op_sel:[0,0,0,1]
	v_cvt_scalef32_pk_fp8_f32 v135, v72, v73, s36 op_sel:[0,0,0,1]
	v_cvt_scalef32_pk_fp8_f32 v136, v76, v77, s36 op_sel:[0,0,0,1]
	v_cvt_scalef32_pk_fp8_f32 v137, v80, v81, s36 op_sel:[0,0,0,1]
	s_waitcnt lgkmcnt(0)
	v_mfma_f32_32x32x64_f8f6f4 v[82:97], v[98:105], v[114:121], 0
	ds_read_b128 v[154:157], v219 offset:5120
	ds_read_b128 v[158:161], v219 offset:5136
	ds_read_b128 v[146:149], v219 offset:7680
	ds_read_b128 v[150:153], v219 offset:7696
	s_cmpk_gt_i32 s42, 0x1ff
	s_cbranch_scc1 .Lmy_rd0_ldum
	s_add_i32 s72, s61, -1
	s_cmp_lt_u32 s72, 16
	s_cbranch_scc0 .Lmy_rd0_noc
	s_waitcnt vmcnt(4)
	v_cvt_scalef32_pk_fp8_f32 v236, v236, v240, s62
	v_cvt_scalef32_pk_fp8_f32 v237, v237, v241, s62
	v_cvt_scalef32_pk_fp8_f32 v238, v238, v242, s62
	v_cvt_scalef32_pk_fp8_f32 v239, v239, v243, s62
	v_cvt_scalef32_pk_fp8_f32 v236, v244, v248, s62 op_sel:[0,0,0,1]
	v_cvt_scalef32_pk_fp8_f32 v237, v245, v249, s62 op_sel:[0,0,0,1]
	v_cvt_scalef32_pk_fp8_f32 v238, v246, v250, s62 op_sel:[0,0,0,1]
	v_cvt_scalef32_pk_fp8_f32 v239, v247, v251, s62 op_sel:[0,0,0,1]
	ds_write_b32 v252, v236
	ds_write_b32 v252, v237 offset:36
	ds_write_b32 v252, v238 offset:72
	ds_write_b32 v252, v239 offset:108
.Lmy_rd0_noc:
	ds_read2_b32 v[244:245], v253 offset1:1
	ds_read2_b32 v[246:247], v253 offset0:2 offset1:3
	s_cmpk_gt_i32 s42, 0x1ff
	s_cbranch_scc1 .Lmy_rd0_sdum
	s_add_i32 s72, s61, -2
	s_cmp_lt_u32 s72, 16
	s_cbranch_scc0 .Lmy_rd0_sdum
	s_andn2_b32 s73, s65, 1
	s_add_u32 s82, s70, s73
	s_addc_u32 s83, s71, 0
	s_bitcmp1_b32 s65, 0
	s_cbranch_scc1 .Lmy_rd0_sdn
	s_waitcnt lgkmcnt(0)
	global_store_dwordx4 v254, v[244:247], s[82:83]
	s_branch .Lmy_rd0_sdone

; DI void attn_unit_a8(unsigned char* lds, const AttnArgs& a) {
;     ...
;     auto w_issue = [&](int j) __attribute__((always_inline)) { const float* src; unsigned char* dst; int ld, n0, k0; bool gu; w_decode(j, src, dst, ld, n0, k0, gu);
;         const float* p = src + (size_t)(k0 + 4 * wid) * ld + n0 + wn4;
;         wq[0] = __builtin_nontemporal_load((const f32x4*)p); wq[1] = __builtin_nontemporal_load((const f32x4*)(p + ld));
;         wq[2] = __builtin_nontemporal_load((const f32x4*)(p + (size_t)2 * ld)); wq[3] = __builtin_nontemporal_load((const f32x4*)(p + (size_t)3 * ld)); };
.Lmy_rd0_sdone:
	s_cmpk_gt_i32 s42, 0x1ff
	s_cbranch_scc1 .Lmy_rd0_ld0
	s_cmp_lt_u32 s61, 16
	s_cbranch_scc1 .Lmy_rd0_lgo

; DI void attn_unit_a8(unsigned char* lds, const AttnArgs& a) {
;     ...
;     auto w_cvt = [&]() __attribute__((always_inline)) { unsigned char* t8 = lds + AT_WT + wn4 * WPITCH + 4 * wid;
; #pragma unroll
;         for (int j = 0; j < 4; ++j) *(unsigned*)(t8 + j * WPITCH) = pk4_fp8_mul64(wq[0][j], wq[1][j], wq[2][j], wq[3][j]); };
;     const int wcol = tid >> 1, whalf = tid & 1;
;     const unsigned wper_gu = (unsigned)((wcol >> 7) * 256 + (wcol & 96) + invperm32(wcol & 31)) * 1024u + 16u * whalf;
;     const unsigned wper_dn = (unsigned)fwd_lane16(wcol) * 1024u + 16u * whalf;
;     auto w_store = [&](int j) __attribute__((always_inline)) { const float* src; unsigned char* dst; int ld, n0, k0; bool gu; w_decode(j, src, dst, ld, n0, k0, gu);
;         const int nb = n0 >> 8; const unsigned uni = (unsigned)(gu ? (nb & 3) * 512 + (nb >> 2) * 128 : nb * 256) * 1024u + (unsigned)k0;
;         const unsigned off = (gu ? wper_gu : wper_dn) + uni;
;         const unsigned* t = (const unsigned*)(lds + AT_WT + wcol * WPITCH + 16 * whalf);
;         *(u32x4*)(dst + off) = (u32x4){t[0], t[1], t[2], t[3]}; };
;     ...
;     auto step = [&](int t, u32x2& kl, u32x2& vl, const u32x2& ks, const u32x2& vs, f32x16& c0, f32x16& c1, f32x16& n0, f32x16& n1, const int hk, const int wj) __attribute__((always_inline)) {
;         const int slot1 = slot == 2 ? 0 : slot + 1, slot2 = slot1 == 2 ? 0 : slot1 + 1;
;         if (hk == 1) { w_cvt(); w_issue(wj + 1 < AT_NWT ? wj + 1 : AT_NWT - 1); }
;         if (hk == 2) w_store(wj);
;         { const int tn = t + 3; gload(tn < a.t1 ? tn : a.t1 - 1, kl, vl); }
;         const unsigned char* Kb = lds + slot * AT_BUFB; const unsigned char* Kn = lds + slot1 * AT_BUFB;
;         const v8i k0 = kread(Kn, 0), k1 = kread(Kn, 1), v0 = vread(Kb, 0), v1 = vread(Kb, 1);
;         n0 = mfma8(k0, qf8, cinit); n1 = mfma8(k1, qf8, cinit);
;         expsum(c0); expsum(c1);
;         const v8i P = pack8(c0, c1);
;         o0[0] = mfma8(v0, P, o0[0]); o0[1] = mfma8(v1, P, o0[1]);
;         lstore(slot2, ks, vs);
;         __syncthreads();
;         slot = slot1;
;     };
;     {
;         int t = a.t0;
;         if (wrider)
;             for (int j = 0; j < AT_NWT; ++j, t += 2) { step(t, kregB, vregB, kregA, vregA, sx0, sx1, sy0, sy1, 1, j); step(t + 1, kregA, vregA, kregB, vregB, sy0, sy1, sx0, sx1, 2, j); }
.LBB0_702:
	s_lshl_b32 s4, s14, 1
	s_waitcnt lgkmcnt(0)
	s_lshr_b32 s12, s14, 3
	s_and_b32 s4, s4, 0x600
	s_and_b32 s12, s12, 0x80
	s_or_b32 s4, s4, s12
	s_and_b64 s[10:11], s[10:11], exec
	s_cselect_b32 s4, s4, s14
	s_and_b32 s10, s24, 3
	s_add_i32 s10, s63, s10
	s_lshl_b32 s10, s10, 5
	s_lshl_b32 s4, s4, 10
	s_add_i32 s15, s4, s10
	s_min_i32 s4, s56, 63
	s_cmp_lt_u32 s56, 60
	s_cselect_b64 s[10:11], -1, 0
	s_lshl_b32 s4, s4, 6
	v_pk_add_f32 v[48:49], v[146:147], v[110:111]
	s_add_i32 s14, s4, 0x100
	s_add_i32 s63, s4, 0xfffff100
	v_pk_add_f32 v[46:47], v[150:151], v[108:109]
	v_pk_add_f32 v[48:49], v[148:149], v[48:49]
	s_and_b64 s[12:13], s[10:11], exec
	v_pk_add_f32 v[46:47], v[142:143], v[46:47]
	v_pk_add_f32 v[48:49], v[58:59], v[48:49]
	s_cselect_b32 s12, s14, s63
	s_add_i32 s25, s25, 1
	v_pk_add_f32 v[46:47], v[144:145], v[46:47]
	v_pk_add_f32 v[48:49], v[60:61], v[48:49]
	s_and_b64 s[6:7], s[6:7], exec
	v_pk_add_f32 v[46:47], v[52:53], v[46:47]
	v_pk_add_f32 v[48:49], v[50:51], v[48:49]
	s_cselect_b32 s14, 0, s25
	v_pk_add_f32 v[46:47], v[56:57], v[46:47]
	v_pk_add_f32 v[48:49], v[54:55], v[48:49]
	s_mul_i32 s6, s14, 0x4680
	v_pk_add_f32 v[38:39], v[38:39], v[46:47]
	v_pk_add_f32 v[36:37], v[36:37], v[48:49]
	v_add_u32_e32 v48, 0xd808, v163
	v_add_u32_e32 v134, s6, v157
	v_pk_add_f32 v[50:51], v[42:43], v[38:39]
	v_pk_add_f32 v[108:109], v[40:41], v[36:37]
	v_add_u32_e32 v45, 0xd800, v163
	ds_read_b128 v[36:39], v134
	ds_read_b128 v[40:43], v134 offset:16
	ds_read2_b32 v[46:47], v45 offset1:1
	ds_read2_b32 v[48:49], v48 offset1:1
	v_pk_add_f32 v[110:111], v[34:35], v[50:51]
	v_add_u32_e32 v34, v44, v158
	v_lshl_or_b32 v34, v34, 10, v160
	v_add_u32_e32 v34, s15, v34
	s_waitcnt lgkmcnt(0)
	global_store_dwordx4 v34, v[46:49], s[8:9]
	v_add_u32_e32 v34, s12, v154
	s_and_b64 s[8:9], s[10:11], exec
	v_ashrrev_i32_e32 v35, 31, v34
	s_cselect_b32 s9, s59, s61
	s_cselect_b32 s8, s58, s60
	v_lshlrev_b64 v[34:35], 7, v[34:35]
	v_mfma_f32_32x32x64_f8f6f4 v[50:65], v[36:43], v[98:105], 0
	v_lshl_add_u64 v[42:43], s[8:9], 0, v[34:35]
	v_lshl_add_u64 v[42:43], v[42:43], 0, v[130:131]
	ds_read_b128 v[34:37], v134 offset:2560
	ds_read_b128 v[38:41], v134 offset:2576
	global_load_dwordx2 v[134:135], v[42:43], off
	v_lshl_add_u64 v[42:43], v[132:133], 0, s[4:5]
	global_load_dwordx2 v[136:137], v[42:43], off offset:256
	v_exp_f32_e32 v82, v82
	v_exp_f32_e32 v83, v83
	v_exp_f32_e32 v86, v86
	v_exp_f32_e32 v87, v87
	v_exp_f32_e32 v90, v90
	v_exp_f32_e32 v91, v91
	v_exp_f32_e32 v94, v94
	v_exp_f32_e32 v95, v95
	v_exp_f32_e32 v150, v66
	v_exp_f32_e32 v151, v67
	v_exp_f32_e32 v174, v70
	v_exp_f32_e32 v175, v71
	v_exp_f32_e32 v74, v74
	v_exp_f32_e32 v75, v75
	v_exp_f32_e32 v78, v78
	v_exp_f32_e32 v79, v79
	ds_read_b128 v[142:145], v164 offset:5120
	ds_read_b128 v[146:149], v164 offset:5136
	ds_read_b128 v[166:169], v164 offset:7680
	ds_read_b128 v[170:173], v164 offset:7696
	v_exp_f32_e32 v84, v84
	v_exp_f32_e32 v85, v85
	v_exp_f32_e32 v88, v88
	v_exp_f32_e32 v89, v89
	v_exp_f32_e32 v92, v92
	v_exp_f32_e32 v93, v93
	v_exp_f32_e32 v96, v96
	v_exp_f32_e32 v97, v97
	v_exp_f32_e32 v164, v68
	v_exp_f32_e32 v165, v69
	v_exp_f32_e32 v176, v72
	v_exp_f32_e32 v177, v73
	v_exp_f32_e32 v76, v76
	v_exp_f32_e32 v77, v77
	v_exp_f32_e32 v80, v80
	v_exp_f32_e32 v81, v81
	s_nop 0
	s_nop 0
	s_nop 0
	s_nop 0
	s_nop 0
	s_nop 0
	s_nop 0
	s_nop 0
	v_cvt_scalef32_pk_fp8_f32 v66, v82, v83, s48
	v_cvt_scalef32_pk_fp8_f32 v70, v150, v151, s48
	v_cvt_scalef32_pk_fp8_f32 v67, v86, v87, s48
	v_cvt_scalef32_pk_fp8_f32 v71, v174, v175, s48
	v_cvt_scalef32_pk_fp8_f32 v68, v90, v91, s48
	v_cvt_scalef32_pk_fp8_f32 v72, v74, v75, s48
	v_cvt_scalef32_pk_fp8_f32 v69, v94, v95, s48
	v_cvt_scalef32_pk_fp8_f32 v73, v78, v79, s48
	v_cvt_scalef32_pk_fp8_f32 v66, v84, v85, s48 op_sel:[0,0,0,1]
	v_cvt_scalef32_pk_fp8_f32 v70, v164, v165, s48 op_sel:[0,0,0,1]
	v_cvt_scalef32_pk_fp8_f32 v67, v88, v89, s48 op_sel:[0,0,0,1]
	v_cvt_scalef32_pk_fp8_f32 v71, v176, v177, s48 op_sel:[0,0,0,1]
	v_cvt_scalef32_pk_fp8_f32 v68, v92, v93, s48 op_sel:[0,0,0,1]
	v_cvt_scalef32_pk_fp8_f32 v72, v76, v77, s48 op_sel:[0,0,0,1]
	v_cvt_scalef32_pk_fp8_f32 v69, v96, v97, s48 op_sel:[0,0,0,1]
	v_cvt_scalef32_pk_fp8_f32 v73, v80, v81, s48 op_sel:[0,0,0,1]
	s_waitcnt lgkmcnt(4)
	v_mfma_f32_32x32x64_f8f6f4 v[34:49], v[34:41], v[98:105], 0
	v_add_f32_e64 v110, v110, v82
	v_add_f32_e64 v111, v111, v83
	v_add_f32_e64 v82, v108, v84
	v_add_f32_e64 v83, v109, v85
	v_add_f32_e64 v84, v86, v110
	v_add_f32_e64 v85, v87, v111
	v_add_f32_e64 v82, v88, v82
	v_add_f32_e64 v83, v89, v83
	s_addk_i32 s6, 0x4680
	v_add_f32_e64 v84, v90, v84
	v_add_f32_e64 v85, v91, v85
	v_add_f32_e64 v82, v92, v82
	v_add_f32_e64 v83, v93, v83
	s_cmp_lg_u32 s14, 2
	v_pk_add_f32 v[82:83], v[96:97], v[82:83]
	v_pk_add_f32 v[84:85], v[94:95], v[84:85]
	s_cselect_b32 s4, s6, 0
	v_pk_add_f32 v[84:85], v[150:151], v[84:85]
	v_pk_add_f32 v[82:83], v[164:165], v[82:83]
	s_add_i32 s4, s4, 0
	v_pk_add_f32 v[82:83], v[176:177], v[82:83]
	s_waitcnt lgkmcnt(2)
	v_mfma_f32_32x32x64_f8f6f4 v[18:33], v[142:149], v[66:73], v[18:33]
	v_add_f32_e64 v84, v174, v84
	v_add_f32_e64 v85, v175, v85
	v_add_f32_e64 v76, v76, v82
	v_add_f32_e64 v77, v77, v83
	v_add_f32_e64 v74, v74, v84
	v_add_f32_e64 v75, v75, v85
	s_add_i32 s24, s24, 1
	s_add_i32 s56, s56, 2
	s_addk_i32 s19, 0x80
	v_add_f32_e64 v110, v80, v76
	v_add_f32_e64 v111, v81, v77
	v_add_f32_e64 v108, v78, v74
	v_add_f32_e64 v109, v79, v75
	s_cmp_lg_u32 s24, 8
	s_waitcnt lgkmcnt(0)
	v_mfma_f32_32x32x64_f8f6f4 v[2:17], v[166:173], v[66:73], v[2:17]
	v_add_u32_e32 v66, s4, v155
	s_waitcnt vmcnt(4)
	ds_write_b64 v66, v[138:139]
	v_add_u32_e32 v66, s4, v156
	v_add_u32_e32 v66, 0x1400, v66
	s_waitcnt vmcnt(3)
	ds_write2_b32 v66, v140, v141 offset1:8
	s_waitcnt lgkmcnt(0)
	s_barrier
	s_cbranch_scc0 .LBB0_712
.LBB0_703:
	s_min_u32 s15, s24, 6
	s_add_i32 s15, s15, 1
	s_lshl_b32 s4, s15, 7
	s_and_b32 s4, s4, 0x1e00
	s_nop 0
	s_nop 0
	s_add_i32 s6, s4, s62
	v_cvt_scalef32_pk_fp8_f32 v66, v116, v112, s47
	v_cvt_scalef32_pk_fp8_f32 v67, v117, v113, s47
	s_mul_hi_u32 s4, s6, 0xaaaaaaab
	v_cvt_scalef32_pk_fp8_f32 v66, v120, v124, s47 op_sel:[0,0,0,1]
	v_cvt_scalef32_pk_fp8_f32 v67, v121, v125, s47 op_sel:[0,0,0,1]
	v_add_u32_e32 v68, 0xd800, v162
	s_lshr_b32 s4, s4, 6
	ds_write2_b32 v68, v66, v67 offset1:9
	s_nop 0
	s_nop 0
	s_mul_i32 s63, s4, 0xffffffa0
	v_cvt_scalef32_pk_fp8_f32 v66, v118, v114, s47
	v_cvt_scalef32_pk_fp8_f32 v67, v119, v115, s47
	s_add_i32 s63, s63, s6
	v_cvt_scalef32_pk_fp8_f32 v66, v122, v126, s47 op_sel:[0,0,0,1]
	v_cvt_scalef32_pk_fp8_f32 v67, v123, v127, s47 op_sel:[0,0,0,1]
	s_mov_b64 s[10:11], s[0:1]
	s_cmp_gt_i32 s63, 63
	s_mov_b64 s[12:13], -1
	ds_write2_b32 v68, v66, v67 offset0:18 offset1:27
	s_cbranch_scc0 .LBB0_705
	s_load_dwordx2 s[6:7], s[10:11], 0xc0
	s_lshl_b64 s[8:9], s[4:5], 22
	s_mov_b64 s[12:13], 0
	s_waitcnt lgkmcnt(0)
	s_add_u32 s6, s6, s8
	s_addc_u32 s7, s7, s9
	s_and_b32 s8, s63, 0x7ffffffc
	s_sub_i32 s25, s8, 64

; DI f32x16 mfma8(v8i a, v8i b, f32x16 c) { return __builtin_amdgcn_mfma_scale_f32_32x32x64_f8f6f4(a, b, c, 0, 0, 0, 0, 0, 0); }
; DI void attn_unit_d8(unsigned char* lds, const AttnArgs& a) {
;     ...
;     auto tile = [&](const unsigned char* Kb, const unsigned char* Kn, v8i& Pa, v8i& Pb, v8i& v0, v8i& v1, const v8i& Qa, const v8i& Qb, const v8i& w0, const v8i& w1) __attribute__((always_inline)) {
;         qk(Kb, 1, s1a, s1b);
;         v0 = rd32(Kb + voff); v1 = rd32(Kb + voff + 32 * A8_PITCH);
;         o0[0] = mfma8(w0, Qa, o0[0]); o1[0] = mfma8(w0, Qb, o1[0]); o0[1] = mfma8(w1, Qa, o0[1]); o1[1] = mfma8(w1, Qb, o1[1]);
;         expsum(s0a, l0); expsum(s0b, l1); pack4(s0a, Pa, 0); pack4(s0b, Pb, 0);
;         qk(Kn, 0, s0a, s0b);
;         expsum(s1a, l0); expsum(s1b, l1); pack4(s1a, Pa, 4); pack4(s1b, Pb, 4);
; #pragma unroll
;         for (int i = 0; i < 8; ++i) { __builtin_amdgcn_sched_group_barrier(0x008, 1, 0); __builtin_amdgcn_sched_group_barrier(0x402, 22, 0); }
;     };
;     for (int t = a.t0; t < a.t1; t += 2) {
;         const int s1 = sb + 1 >= 5 ? sb - 4 : sb + 1, s2 = sb + 2 >= 5 ? sb - 3 : sb + 2, s3 = sb + 3 >= 5 ? sb - 2 : sb + 3, s4 = sb + 4 >= 5 ? sb - 1 : sb + 4;
;         { const int ta = t + 3, tb = t + 4; gload(ta < a.t1 ? ta : a.t1 - 1, kreg0, vreg0); gload(tb < a.t1 ? tb : a.t1 - 1, kreg1, vreg1); }
;         tile(lds + sb * D8_SLOT, lds + s1 * D8_SLOT, PaX, PbX, vX0, vX1, PaY, PbY, vY0, vY1);
;         tile(lds + s1 * D8_SLOT, lds + s2 * D8_SLOT, PaY, PbY, vY0, vY1, PaX, PbX, vX0, vX1);
.LBB0_1888:
	s_add_i32 s22, s22, 2
	s_mul_i32 s8, s23, 0x2800
	s_cmp_gt_i32 s23, 3
	v_mfma_f32_32x32x64_f8f6f4 v[50:65], v[154:161], v[138:145], v[50:65]
	v_exp_f32_e32 v194, v90
	v_add_u32_e32 v90, s8, v219
	s_cselect_b32 s8, -4, 1
	s_add_i32 s51, s8, s23
	s_cmp_gt_i32 s23, 2
	s_cselect_b32 s8, -3, 2
	s_add_i32 s8, s8, s23
	s_cmp_gt_i32 s23, 1
	s_cselect_b32 s52, -2, 3
	s_add_i32 s52, s52, s23
	s_cmp_gt_i32 s23, 0
	s_cselect_b32 s53, -1, 4
	s_min_u32 s56, s22, 64
	s_add_i32 s53, s53, s23
	s_cmp_lt_u32 s22, 61
	s_mul_i32 s50, s8, 0x2800
	s_mov_b32 s23, s8
	s_cselect_b64 s[54:55], -1, 0
	s_lshl_b32 s8, s56, 6
	s_add_i32 s56, s8, 0xc0
	s_add_i32 s57, s8, 0xfffff0c0
	s_and_b64 s[54:55], s[54:55], exec
	v_lshl_add_u64 v[98:99], v[184:185], 0, s[8:9]
	s_cselect_b32 s8, s56, s57
	s_cselect_b32 s55, s19, s21
	s_cselect_b32 s54, s18, s20
	s_min_u32 s58, s22, 63
	v_exp_f32_e32 v200, v82
	v_exp_f32_e32 v201, v83
	v_exp_f32_e32 v198, v84
	v_exp_f32_e32 v199, v85
	v_exp_f32_e32 v202, v86
	v_exp_f32_e32 v203, v87
	v_exp_f32_e32 v196, v88
	v_exp_f32_e32 v197, v89
	ds_read_b128 v[82:85], v90 offset:2560
	ds_read_b128 v[86:89], v90 offset:2576
	global_load_dwordx2 v[204:205], v[98:99], off offset:192
	v_add_u32_e32 v98, s8, v182
	s_cmp_lt_u32 s22, 60
	v_ashrrev_i32_e32 v99, 31, v98
	s_cselect_b64 s[56:57], -1, 0
	s_lshl_b32 s8, s58, 6
	v_lshlrev_b64 v[98:99], 8, v[98:99]
	s_add_i32 s58, s8, 0x100
	s_add_i32 s59, s8, 0xfffff100
	v_lshl_add_u64 v[98:99], s[54:55], 0, v[98:99]
	s_and_b64 s[54:55], s[56:57], exec
	v_lshl_add_u64 v[100:101], v[184:185], 0, s[8:9]
	s_cselect_b32 s8, s58, s59
	v_lshl_add_u64 v[220:221], v[98:99], 0, v[178:179]
	v_add_u32_e32 v98, s8, v182
	v_ashrrev_i32_e32 v99, 31, v98
	s_cselect_b32 s55, s19, s21
	s_cselect_b32 s54, s18, s20
	v_lshlrev_b64 v[98:99], 8, v[98:99]
	v_lshl_add_u64 v[98:99], s[54:55], 0, v[98:99]
	global_load_dwordx2 v[206:207], v[100:101], off offset:256
	v_lshl_add_u64 v[222:223], v[98:99], 0, v[178:179]
	s_waitcnt lgkmcnt(0)
	v_mfma_f32_32x32x64_f8f6f4 v[98:113], v[82:89], v[114:121], 0
	v_exp_f32_e32 v195, v91
	v_exp_f32_e32 v224, v92
	v_exp_f32_e32 v225, v93
	v_exp_f32_e32 v226, v94
	v_exp_f32_e32 v227, v95
	v_exp_f32_e32 v228, v96
	v_exp_f32_e32 v229, v97
	ds_read_b128 v[170:173], v90 offset:5120
	ds_read_b128 v[174:177], v90 offset:5136
	ds_read_b128 v[162:165], v90 offset:7680
	ds_read_b128 v[166:169], v90 offset:7696
	v_pk_add_f32 v[90:91], v[188:189], v[200:201]
	v_pk_add_f32 v[92:93], v[186:187], v[198:199]
	v_pk_add_f32 v[90:91], v[202:203], v[90:91]
	v_pk_add_f32 v[92:93], v[196:197], v[92:93]
	v_pk_add_f32 v[90:91], v[194:195], v[90:91]
	v_pk_add_f32 v[92:93], v[224:225], v[92:93]
	v_exp_f32_e32 v66, v66
	v_exp_f32_e32 v67, v67
	v_exp_f32_e32 v68, v68
	v_exp_f32_e32 v69, v69
	v_exp_f32_e32 v70, v70
	v_exp_f32_e32 v71, v71
	v_exp_f32_e32 v72, v72
	v_pk_add_f32 v[230:231], v[228:229], v[92:93]
	v_pk_add_f32 v[232:233], v[226:227], v[90:91]
	v_mfma_f32_32x32x64_f8f6f4 v[82:97], v[82:89], v[122:129], 0
	v_exp_f32_e32 v73, v73
	v_exp_f32_e32 v74, v74
	v_exp_f32_e32 v75, v75
	v_exp_f32_e32 v76, v76
	v_exp_f32_e32 v77, v77
	v_exp_f32_e32 v78, v78
	v_exp_f32_e32 v79, v79
	v_exp_f32_e32 v80, v80
	v_exp_f32_e32 v81, v81
	v_pk_add_f32 v[188:189], v[192:193], v[66:67]
	v_pk_add_f32 v[190:191], v[190:191], v[68:69]
	s_nop 0
	v_pk_add_f32 v[188:189], v[70:71], v[188:189]
	v_pk_add_f32 v[190:191], v[72:73], v[190:191]
	s_nop 0
	v_cvt_scalef32_pk_fp8_f32 v186, v200, v201, s36
	v_pk_add_f32 v[188:189], v[74:75], v[188:189]
	v_pk_add_f32 v[190:191], v[76:77], v[190:191]
	v_cvt_scalef32_pk_fp8_f32 v187, v202, v203, s36
	v_cvt_scalef32_pk_fp8_f32 v186, v198, v199, s36 op_sel:[0,0,0,1]
	v_pk_add_f32 v[192:193], v[78:79], v[188:189]
	v_pk_add_f32 v[190:191], v[80:81], v[190:191]
	v_mfma_f32_32x32x64_f8f6f4 v[2:17], v[154:161], v[130:137], v[2:17]
	s_nop 0
	s_nop 0
	s_nop 0
	s_nop 0
	s_nop 0
	s_nop 0
	s_mulk_i32 s51, 0x2800
	v_cvt_scalef32_pk_fp8_f32 v188, v194, v195, s36
	v_cvt_scalef32_pk_fp8_f32 v189, v226, v227, s36
	v_cvt_scalef32_pk_fp8_f32 v154, v66, v67, s36
	v_cvt_scalef32_pk_fp8_f32 v155, v70, v71, s36
	v_cvt_scalef32_pk_fp8_f32 v156, v74, v75, s36
	v_cvt_scalef32_pk_fp8_f32 v157, v78, v79, s36
	v_cvt_scalef32_pk_fp8_f32 v187, v196, v197, s36 op_sel:[0,0,0,1]
	v_add_u32_e32 v234, s51, v219
	v_cvt_scalef32_pk_fp8_f32 v188, v224, v225, s36 op_sel:[0,0,0,1]
	v_cvt_scalef32_pk_fp8_f32 v189, v228, v229, s36 op_sel:[0,0,0,1]
	v_cvt_scalef32_pk_fp8_f32 v154, v68, v69, s36 op_sel:[0,0,0,1]
	v_cvt_scalef32_pk_fp8_f32 v155, v72, v73, s36 op_sel:[0,0,0,1]
	v_cvt_scalef32_pk_fp8_f32 v156, v76, v77, s36 op_sel:[0,0,0,1]
	v_cvt_scalef32_pk_fp8_f32 v157, v80, v81, s36 op_sel:[0,0,0,1]
	v_exp_f32_e32 v98, v98
	v_exp_f32_e32 v99, v99
	v_mfma_f32_32x32x64_f8f6f4 v[34:49], v[146:153], v[138:145], v[34:49]
	v_exp_f32_e32 v100, v100
	v_exp_f32_e32 v101, v101
	v_exp_f32_e32 v102, v102
	v_exp_f32_e32 v103, v103
	v_exp_f32_e32 v104, v104
	v_exp_f32_e32 v105, v105
	v_exp_f32_e32 v106, v106
	v_exp_f32_e32 v107, v107
	v_exp_f32_e32 v108, v108
	v_exp_f32_e32 v109, v109
	v_exp_f32_e32 v110, v110
	v_exp_f32_e32 v111, v111
	v_exp_f32_e32 v112, v112
	v_exp_f32_e32 v113, v113
	ds_read_b128 v[194:197], v234
	ds_read_b128 v[198:201], v234 offset:16
	v_pk_add_f32 v[66:67], v[232:233], v[98:99]
	v_pk_add_f32 v[68:69], v[230:231], v[100:101]
	v_pk_add_f32 v[66:67], v[102:103], v[66:67]
	v_pk_add_f32 v[68:69], v[104:105], v[68:69]
	v_pk_add_f32 v[66:67], v[106:107], v[66:67]
	v_pk_add_f32 v[68:69], v[108:109], v[68:69]
	v_pk_add_f32 v[140:141], v[110:111], v[66:67]
	v_pk_add_f32 v[138:139], v[112:113], v[68:69]
	v_mfma_f32_32x32x64_f8f6f4 v[18:33], v[146:153], v[130:137], v[18:33]
	v_exp_f32_e32 v82, v82
	v_exp_f32_e32 v83, v83
	v_exp_f32_e32 v84, v84
	v_exp_f32_e32 v85, v85
	v_exp_f32_e32 v86, v86
	v_exp_f32_e32 v87, v87
	v_exp_f32_e32 v88, v88
	v_exp_f32_e32 v89, v89
	v_exp_f32_e32 v90, v90
	v_exp_f32_e32 v91, v91
	v_exp_f32_e32 v92, v92
	v_exp_f32_e32 v93, v93
	v_exp_f32_e32 v94, v94
	v_exp_f32_e32 v95, v95
	v_exp_f32_e32 v96, v96
	v_exp_f32_e32 v97, v97
	v_pk_add_f32 v[66:67], v[192:193], v[82:83]
	v_pk_add_f32 v[68:69], v[190:191], v[84:85]
	v_pk_add_f32 v[66:67], v[86:87], v[66:67]
	v_pk_add_f32 v[68:69], v[88:89], v[68:69]
	v_pk_add_f32 v[130:131], v[90:91], v[66:67]
	v_pk_add_f32 v[132:133], v[92:93], v[68:69]
	s_waitcnt lgkmcnt(0)
; DI KParamsPtr kparams() { KParamsPtr p = (KParamsPtr)__builtin_amdgcn_kernarg_segment_ptr(); asm volatile("" : "+s"(p)); return p; }
; DI f32x16 mfma8(v8i a, v8i b, f32x16 c) { return __builtin_amdgcn_mfma_scale_f32_32x32x64_f8f6f4(a, b, c, 0, 0, 0, 0, 0, 0); }
; DI void attn_unit_a8(unsigned char* lds, const AttnArgs& a) {
;     ...
;     auto w_decode = [&](int j, const float*& src, unsigned char*& dst, int& ld, int& n0, int& k0, bool& gu) __attribute__((always_inline)) {
;         const int g = (j >> 2) * 512 + a.wl, e = g / 96, rr = g - e * 96; KParamsPtr kp = kparams();
;         if (rr < 64) { src = kp->w_gu + ((size_t)a.wli * NE + e) * (1024 * 2048); dst = kp->ws + WS_WGU + (size_t)a.wli * SZ_WGU + (size_t)e * 2048 * 1024; ld = 2048; n0 = (rr & 7) * 256; k0 = ((rr >> 3) * 4 + (j & 3)) * 32; gu = true; }
;         else { const int q = rr - 64; src = kp->w_dn + ((size_t)a.wli * NE + e) * (1024 * 1024); dst = kp->ws + WS_WDN + (size_t)a.wli * SZ_WDN + (size_t)e * 1024 * 1024; ld = 1024; n0 = (q & 3) * 256; k0 = ((q >> 2) * 4 + (j & 3)) * 32; gu = false; } };
; DI void attn_unit_d8(unsigned char* lds, const AttnArgs& a) {
;     ...
;     auto tile = [&](const unsigned char* Kb, const unsigned char* Kn, v8i& Pa, v8i& Pb, v8i& v0, v8i& v1, const v8i& Qa, const v8i& Qb, const v8i& w0, const v8i& w1) __attribute__((always_inline)) {
;         qk(Kb, 1, s1a, s1b);
;         v0 = rd32(Kb + voff); v1 = rd32(Kb + voff + 32 * A8_PITCH);
;         o0[0] = mfma8(w0, Qa, o0[0]); o1[0] = mfma8(w0, Qb, o1[0]); o0[1] = mfma8(w1, Qa, o0[1]); o1[1] = mfma8(w1, Qb, o1[1]);
;         expsum(s0a, l0); expsum(s0b, l1); pack4(s0a, Pa, 0); pack4(s0b, Pb, 0);
;         qk(Kn, 0, s0a, s0b);
;         expsum(s1a, l0); expsum(s1b, l1); pack4(s1a, Pa, 4); pack4(s1b, Pb, 4);
; #pragma unroll
;         for (int i = 0; i < 8; ++i) { __builtin_amdgcn_sched_group_barrier(0x008, 1, 0); __builtin_amdgcn_sched_group_barrier(0x402, 22, 0); }
;     };
	v_mfma_f32_32x32x64_f8f6f4 v[66:81], v[194:201], v[114:121], 0
	s_nop 0
	s_nop 0
	s_nop 0
	s_nop 0
	s_nop 0
	s_nop 0
	s_nop 0
	v_cvt_scalef32_pk_fp8_f32 v190, v98, v99, s36
	v_cvt_scalef32_pk_fp8_f32 v191, v102, v103, s36
	v_cvt_scalef32_pk_fp8_f32 v192, v106, v107, s36
	v_cvt_scalef32_pk_fp8_f32 v193, v110, v111, s36
	v_cvt_scalef32_pk_fp8_f32 v158, v82, v83, s36
	v_cvt_scalef32_pk_fp8_f32 v159, v86, v87, s36
	v_pk_add_f32 v[142:143], v[96:97], v[132:133]
	v_pk_add_f32 v[144:145], v[94:95], v[130:131]
	v_cvt_scalef32_pk_fp8_f32 v160, v90, v91, s36
	v_cvt_scalef32_pk_fp8_f32 v190, v100, v101, s36 op_sel:[0,0,0,1]
	v_cvt_scalef32_pk_fp8_f32 v191, v104, v105, s36 op_sel:[0,0,0,1]
	v_cvt_scalef32_pk_fp8_f32 v192, v108, v109, s36 op_sel:[0,0,0,1]
	v_cvt_scalef32_pk_fp8_f32 v193, v112, v113, s36 op_sel:[0,0,0,1]
	v_cvt_scalef32_pk_fp8_f32 v158, v84, v85, s36 op_sel:[0,0,0,1]
	v_cvt_scalef32_pk_fp8_f32 v159, v88, v89, s36 op_sel:[0,0,0,1]
	v_mfma_f32_32x32x64_f8f6f4 v[98:113], v[194:201], v[122:129], 0
	global_load_dwordx2 v[194:195], v[220:221], off
	global_load_dwordx2 v[196:197], v[222:223], off
	ds_read_b128 v[130:133], v234 offset:2560
	ds_read_b128 v[134:137], v234 offset:2576
	v_exp_f32_e32 v146, v66
	s_lshr_b32 s73, s61, 2
	v_exp_f32_e32 v147, v67
	s_add_i32 s73, s73, 2
	s_mulk_i32 s52, 0x2800
	s_nop 0
	s_add_i32 s8, s52, 0
	v_cvt_scalef32_pk_fp8_f32 v161, v94, v95, s36
	v_add_u32_e32 v224, s8, v183
	v_cvt_scalef32_pk_fp8_f32 v160, v92, v93, s36 op_sel:[0,0,0,1]
	v_cvt_scalef32_pk_fp8_f32 v161, v96, v97, s36 op_sel:[0,0,0,1]
	v_exp_f32_e32 v148, v68
	s_lshl_b32 s73, s73, 9
	v_exp_f32_e32 v149, v69
	s_add_i32 s73, s73, s46
	v_exp_f32_e32 v150, v70
	s_mul_i32 s75, s73, 0xaaab
	v_exp_f32_e32 v151, v71
	s_lshr_b32 s75, s75, 22
	v_exp_f32_e32 v152, v72
	s_mul_i32 s76, s75, 0x60
	v_exp_f32_e32 v153, v73
	s_sub_i32 s76, s73, s76
	v_exp_f32_e32 v198, v74
	s_lshr_b32 s77, s76, 6
	v_exp_f32_e32 v199, v75
	s_lshl_b32 s78, s77, 6
	v_exp_f32_e32 v200, v76
	s_sub_i32 s76, s76, s78
	v_exp_f32_e32 v201, v77
	s_sub_i32 s78, 3, s77
	v_exp_f32_e32 v202, v78
	s_lshr_b32 s79, s76, s78
	v_exp_f32_e32 v203, v79
	s_lshl_b32 s79, s79, 2
	v_exp_f32_e32 v220, v80
	s_and_b32 s81, s61, 3
	v_exp_f32_e32 v221, v81
	s_add_i32 s79, s79, s81
	v_pk_add_f32 v[66:67], v[140:141], v[146:147]
	s_waitcnt lgkmcnt(0)
	v_mfma_f32_32x32x64_f8f6f4 v[82:97], v[130:137], v[114:121], 0
	v_add_f32_e64 v68, v138, v148
	v_add_f32_e64 v69, v139, v149
	v_add_f32_e64 v66, v150, v66
	v_add_f32_e64 v67, v151, v67
	v_add_f32_e64 v68, v152, v68
	v_add_f32_e64 v69, v153, v69
	v_add_f32_e64 v138, v198, v66
	v_add_f32_e64 v139, v199, v67
	v_add_f32_e64 v140, v200, v68
	v_add_f32_e64 v141, v201, v69
	v_exp_f32_e32 v98, v98
	s_lshl_b32 s79, s79, 5
	v_exp_f32_e32 v99, v99
	s_lshl_b32 s81, s63, 2
	v_exp_f32_e32 v100, v100
	s_add_i32 s81, s81, s79
	v_exp_f32_e32 v101, v101
	s_sub_i32 s78, 13, s77
	v_exp_f32_e32 v102, v102
	s_lshl_b32 s81, s81, s78
	v_exp_f32_e32 v103, v103
	s_lshr_b32 s78, 7, s77
	v_exp_f32_e32 v104, v104
	s_and_b32 s78, s76, s78
	v_exp_f32_e32 v105, v105
	s_lshl_b32 s72, s78, 10
	v_exp_f32_e32 v106, v106
	s_add_i32 s81, s81, s72
	v_exp_f32_e32 v107, v107
	s_add_i32 s72, s75, 32
	v_exp_f32_e32 v108, v108
	s_sub_i32 s80, 23, s77
	v_exp_f32_e32 v109, v109
	s_lshl_b32 s72, s72, s80
	v_exp_f32_e32 v110, v110
	s_add_i32 s81, s81, s72
	v_exp_f32_e32 v111, v111
	s_cmp_eq_u32 s77, 0
	s_cselect_b64 s[84:85], s[66:67], s[68:69]
	v_exp_f32_e32 v112, v112
	s_add_u32 s84, s84, s81
	s_addc_u32 s85, s85, 0
	v_exp_f32_e32 v113, v113
	s_lshr_b32 s80, 0x2000, s77
	v_exp_f32_e32 v82, v82
	s_and_b32 s72, s78, 3
	v_mfma_f32_32x32x64_f8f6f4 v[66:81], v[130:137], v[122:129], 0
	v_add_f32_e64 v130, v144, v98
	v_add_f32_e64 v131, v145, v99
	v_add_f32_e64 v132, v142, v100
	v_add_f32_e64 v133, v143, v101
	v_add_f32_e64 v142, v102, v130
	v_add_f32_e64 v143, v103, v131
	v_add_f32_e64 v132, v104, v132
	v_add_f32_e64 v133, v105, v133
	v_add_f32_e64 v134, v220, v140
	v_add_f32_e64 v135, v221, v141
	v_add_f32_e64 v136, v202, v138
	v_add_f32_e64 v137, v203, v139
	s_nop 0
	s_nop 0
	s_nop 0
	s_nop 0
	s_nop 0
	s_nop 0
	v_pk_add_f32 v[142:143], v[106:107], v[142:143]
	v_pk_add_f32 v[132:133], v[108:109], v[132:133]
	v_cvt_scalef32_pk_fp8_f32 v138, v146, v147, s36
	v_cvt_scalef32_pk_fp8_f32 v139, v150, v151, s36
	v_cvt_scalef32_pk_fp8_f32 v140, v198, v199, s36
	v_cvt_scalef32_pk_fp8_f32 v141, v202, v203, s36
	v_cvt_scalef32_pk_fp8_f32 v130, v98, v99, s36
	v_cvt_scalef32_pk_fp8_f32 v131, v102, v103, s36
	v_pk_add_f32 v[146:147], v[112:113], v[132:133]
	v_pk_add_f32 v[150:151], v[110:111], v[142:143]
	v_mfma_f32_32x32x64_f8f6f4 v[50:65], v[170:177], v[186:193], v[50:65]
	v_exp_f32_e32 v83, v83
	s_lshl_b32 s72, s72, 19
	v_exp_f32_e32 v84, v84
	s_lshr_b32 s81, s78, 2
	v_exp_f32_e32 v85, v85
	s_lshl_b32 s81, s81, 17
	v_add_u32_e32 v102, s50, v219
	v_exp_f32_e32 v86, v86
	s_add_i32 s72, s72, s81
	v_exp_f32_e32 v87, v87
	s_lshl_b32 s81, s78, 18
	v_exp_f32_e32 v88, v88
	s_cmp_eq_u32 s77, 0
	s_cselect_b32 s72, s72, s81
; DI void attn_unit_a8(unsigned char* lds, const AttnArgs& a) {
;     ...
;     auto w_cvt = [&]() __attribute__((always_inline)) { unsigned char* t8 = lds + AT_WT + wn4 * WPITCH + 4 * wid;
; #pragma unroll
;         for (int j = 0; j < 4; ++j) *(unsigned*)(t8 + j * WPITCH) = pk4_fp8_mul64(wq[0][j], wq[1][j], wq[2][j], wq[3][j]); };
;     const int wcol = tid >> 1, whalf = tid & 1;
;     const unsigned wper_gu = (unsigned)((wcol >> 7) * 256 + (wcol & 96) + invperm32(wcol & 31)) * 1024u + 16u * whalf;
;     const unsigned wper_dn = (unsigned)fwd_lane16(wcol) * 1024u + 16u * whalf;
;     auto w_store = [&](int j) __attribute__((always_inline)) { const float* src; unsigned char* dst; int ld, n0, k0; bool gu; w_decode(j, src, dst, ld, n0, k0, gu);
;         const int nb = n0 >> 8; const unsigned uni = (unsigned)(gu ? (nb & 3) * 512 + (nb >> 2) * 128 : nb * 256) * 1024u + (unsigned)k0;
; DI void attn_unit_d8(unsigned char* lds, const AttnArgs& a) {
;     ...
;     auto tile = [&](const unsigned char* Kb, const unsigned char* Kn, v8i& Pa, v8i& Pb, v8i& v0, v8i& v1, const v8i& Qa, const v8i& Qb, const v8i& w0, const v8i& w1) __attribute__((always_inline)) {
;         qk(Kb, 1, s1a, s1b);
;         v0 = rd32(Kb + voff); v1 = rd32(Kb + voff + 32 * A8_PITCH);
;         o0[0] = mfma8(w0, Qa, o0[0]); o1[0] = mfma8(w0, Qb, o1[0]); o0[1] = mfma8(w1, Qa, o0[1]); o1[1] = mfma8(w1, Qb, o1[1]);
;         expsum(s0a, l0); expsum(s0b, l1); pack4(s0a, Pa, 0); pack4(s0b, Pb, 0);
;         qk(Kn, 0, s0a, s0b);
;         expsum(s1a, l0); expsum(s1b, l1); pack4(s1a, Pa, 4); pack4(s1b, Pb, 4);
; #pragma unroll
;         for (int i = 0; i < 8; ++i) { __builtin_amdgcn_sched_group_barrier(0x008, 1, 0); __builtin_amdgcn_sched_group_barrier(0x402, 22, 0); }
;     };
;     for (int t = a.t0; t < a.t1; t += 2) {
;         const int s1 = sb + 1 >= 5 ? sb - 4 : sb + 1, s2 = sb + 2 >= 5 ? sb - 3 : sb + 2, s3 = sb + 3 >= 5 ? sb - 2 : sb + 3, s4 = sb + 4 >= 5 ? sb - 1 : sb + 4;
;         { const int ta = t + 3, tb = t + 4; gload(ta < a.t1 ? ta : a.t1 - 1, kreg0, vreg0); gload(tb < a.t1 ? tb : a.t1 - 1, kreg1, vreg1); }
;         tile(lds + sb * D8_SLOT, lds + s1 * D8_SLOT, PaX, PbX, vX0, vX1, PaY, PbY, vY0, vY1);
;         tile(lds + s1 * D8_SLOT, lds + s2 * D8_SLOT, PaY, PbY, vY0, vY1, PaX, PbX, vX0, vX1);
;         lstore(s3, kreg0, vreg0); lstore(s4, kreg1, vreg1);
	v_exp_f32_e32 v89, v89
	s_mul_i32 s81, s77, 0xc000000
	v_cvt_scalef32_pk_fp8_f32 v130, v100, v101, s36 op_sel:[0,0,0,1]
	v_cvt_scalef32_pk_fp8_f32 v131, v104, v105, s36 op_sel:[0,0,0,1]
	v_exp_f32_e32 v90, v90
	s_add_i32 s81, s81, 0x9094000
	v_exp_f32_e32 v91, v91
	s_add_i32 s72, s72, s79
	v_exp_f32_e32 v92, v92
	s_sub_i32 s73, 21, s77
	v_exp_f32_e32 v93, v93
	s_lshl_b32 s73, s75, s73
	ds_read_b128 v[98:101], v102
	ds_read_b128 v[102:105], v102 offset:16
	s_nop 0
	v_cvt_scalef32_pk_fp8_f32 v138, v148, v149, s36 op_sel:[0,0,0,1]
	v_cvt_scalef32_pk_fp8_f32 v139, v152, v153, s36 op_sel:[0,0,0,1]
	v_cvt_scalef32_pk_fp8_f32 v140, v200, v201, s36 op_sel:[0,0,0,1]
	v_cvt_scalef32_pk_fp8_f32 v141, v220, v221, s36 op_sel:[0,0,0,1]
	s_nop 0
	v_exp_f32_e32 v94, v94
	s_add_i32 s72, s72, s73
	v_exp_f32_e32 v95, v95
	s_add_u32 s72, s72, s81
	v_mfma_f32_32x32x64_f8f6f4 v[2:17], v[170:177], v[154:161], v[2:17]
	v_exp_f32_e32 v148, v96
	s_or_b32 s79, s72, s77
	v_cvt_scalef32_pk_fp8_f32 v132, v106, v107, s36
	v_exp_f32_e32 v149, v97
	v_pk_add_f32 v[96:97], v[136:137], v[82:83]
	v_pk_add_f32 v[106:107], v[134:135], v[84:85]
	v_exp_f32_e32 v66, v66
	v_exp_f32_e32 v67, v67
	v_exp_f32_e32 v68, v68
	v_exp_f32_e32 v69, v69
	v_cvt_scalef32_pk_fp8_f32 v133, v110, v111, s36
	v_pk_add_f32 v[106:107], v[88:89], v[106:107]
	v_pk_add_f32 v[96:97], v[86:87], v[96:97]
	v_exp_f32_e32 v70, v70
	v_exp_f32_e32 v71, v71
	v_exp_f32_e32 v72, v72
	v_exp_f32_e32 v73, v73
	v_cvt_scalef32_pk_fp8_f32 v132, v108, v109, s36 op_sel:[0,0,0,1]
	v_cvt_scalef32_pk_fp8_f32 v133, v112, v113, s36 op_sel:[0,0,0,1]
	v_pk_add_f32 v[96:97], v[90:91], v[96:97]
	v_pk_add_f32 v[106:107], v[92:93], v[106:107]
	v_exp_f32_e32 v74, v74
	v_exp_f32_e32 v75, v75
	v_mfma_f32_32x32x64_f8f6f4 v[34:49], v[162:169], v[186:193], v[34:49]
	v_exp_f32_e32 v76, v76
	v_exp_f32_e32 v77, v77
	v_exp_f32_e32 v78, v78
	v_exp_f32_e32 v79, v79
	s_nop 0
	v_exp_f32_e32 v80, v80
	v_exp_f32_e32 v81, v81
	s_nop 0
	s_nop 0
	v_cvt_scalef32_pk_fp8_f32 v142, v82, v83, s36
	s_nop 0
	v_cvt_scalef32_pk_fp8_f32 v143, v86, v87, s36
	v_cvt_scalef32_pk_fp8_f32 v144, v90, v91, s36
	v_cvt_scalef32_pk_fp8_f32 v142, v84, v85, s36 op_sel:[0,0,0,1]
	v_pk_add_f32 v[82:83], v[150:151], v[66:67]
	v_pk_add_f32 v[84:85], v[146:147], v[68:69]
	s_mulk_i32 s53, 0x2800
	v_pk_add_f32 v[186:187], v[148:149], v[106:107]
	v_pk_add_f32 v[188:189], v[94:95], v[96:97]
	v_cvt_scalef32_pk_fp8_f32 v145, v94, v95, s36
	v_cvt_scalef32_pk_fp8_f32 v143, v88, v89, s36 op_sel:[0,0,0,1]
	v_cvt_scalef32_pk_fp8_f32 v144, v92, v93, s36 op_sel:[0,0,0,1]
	v_pk_add_f32 v[84:85], v[72:73], v[84:85]
	v_mfma_f32_32x32x64_f8f6f4 v[18:33], v[162:169], v[154:161], v[18:33]
	v_add_f32_e64 v82, v70, v82
	v_add_f32_e64 v83, v71, v83
	s_nop 0
	s_nop 0
	s_nop 0
	s_nop 0
	s_add_i32 s51, s53, 0
	v_add_f32_e64 v82, v74, v82
	v_add_f32_e64 v83, v75, v83
	v_add_f32_e64 v84, v76, v84
	v_add_f32_e64 v85, v77, v85
	v_cvt_scalef32_pk_fp8_f32 v134, v66, v67, s36
	v_cvt_scalef32_pk_fp8_f32 v135, v70, v71, s36
	v_cvt_scalef32_pk_fp8_f32 v136, v74, v75, s36
	v_cvt_scalef32_pk_fp8_f32 v137, v78, v79, s36
	v_pk_add_f32 v[190:191], v[80:81], v[84:85]
	v_pk_add_f32 v[192:193], v[78:79], v[82:83]
	v_add_u32_e32 v106, s8, v218
	v_add_u32_e32 v107, s51, v183
	v_cvt_scalef32_pk_fp8_f32 v145, v148, v149, s36 op_sel:[0,0,0,1]
	v_cvt_scalef32_pk_fp8_f32 v134, v68, v69, s36 op_sel:[0,0,0,1]
	v_cvt_scalef32_pk_fp8_f32 v135, v72, v73, s36 op_sel:[0,0,0,1]
	v_cvt_scalef32_pk_fp8_f32 v136, v76, v77, s36 op_sel:[0,0,0,1]
	v_cvt_scalef32_pk_fp8_f32 v137, v80, v81, s36 op_sel:[0,0,0,1]
	s_waitcnt lgkmcnt(0)
	v_mfma_f32_32x32x64_f8f6f4 v[82:97], v[98:105], v[114:121], 0
	ds_read_b128 v[154:157], v234 offset:5120
	ds_read_b128 v[158:161], v234 offset:5136
	ds_read_b128 v[146:149], v234 offset:7680
	ds_read_b128 v[150:153], v234 offset:7696
	s_cmpk_gt_i32 s46, 0x1ff
	s_cbranch_scc1 .Lmy_rd1_ldum
	s_add_i32 s72, s61, -1
	s_cmp_lt_u32 s72, 16
	s_cbranch_scc0 .Lmy_rd1_noc
	s_waitcnt vmcnt(4)
	v_cvt_scalef32_pk_fp8_f32 v236, v236, v240, s62
	v_cvt_scalef32_pk_fp8_f32 v237, v237, v241, s62
	v_cvt_scalef32_pk_fp8_f32 v238, v238, v242, s62
	v_cvt_scalef32_pk_fp8_f32 v239, v239, v243, s62
	v_cvt_scalef32_pk_fp8_f32 v236, v244, v248, s62 op_sel:[0,0,0,1]
	v_cvt_scalef32_pk_fp8_f32 v237, v245, v249, s62 op_sel:[0,0,0,1]
	v_cvt_scalef32_pk_fp8_f32 v238, v246, v250, s62 op_sel:[0,0,0,1]
	v_cvt_scalef32_pk_fp8_f32 v239, v247, v251, s62 op_sel:[0,0,0,1]
	ds_write_b32 v252, v236
	ds_write_b32 v252, v237 offset:36
	ds_write_b32 v252, v238 offset:72
	ds_write_b32 v252, v239 offset:108
.Lmy_rd1_noc:
	ds_read2_b32 v[244:245], v253 offset1:1
	ds_read2_b32 v[246:247], v253 offset0:2 offset1:3
	s_cmpk_gt_i32 s46, 0x1ff
	s_cbranch_scc1 .Lmy_rd1_sdum
	s_add_i32 s72, s61, -2
	s_cmp_lt_u32 s72, 16
	s_cbranch_scc0 .Lmy_rd1_sdum
	s_andn2_b32 s73, s65, 1
	s_add_u32 s82, s70, s73
	s_addc_u32 s83, s71, 0
	s_bitcmp1_b32 s65, 0
	s_cbranch_scc1 .Lmy_rd1_sdn
	s_waitcnt lgkmcnt(0)
	global_store_dwordx4 v254, v[244:247], s[82:83]
	s_branch .Lmy_rd1_sdone

; DI void attn_unit_a8(unsigned char* lds, const AttnArgs& a) {
;     ...
;     auto w_issue = [&](int j) __attribute__((always_inline)) { const float* src; unsigned char* dst; int ld, n0, k0; bool gu; w_decode(j, src, dst, ld, n0, k0, gu);
;         const float* p = src + (size_t)(k0 + 4 * wid) * ld + n0 + wn4;
;         wq[0] = __builtin_nontemporal_load((const f32x4*)p); wq[1] = __builtin_nontemporal_load((const f32x4*)(p + ld));
;         wq[2] = __builtin_nontemporal_load((const f32x4*)(p + (size_t)2 * ld)); wq[3] = __builtin_nontemporal_load((const f32x4*)(p + (size_t)3 * ld)); };
.Lmy_rd1_sdone:
	s_cmpk_gt_i32 s46, 0x1ff
	s_cbranch_scc1 .Lmy_rd1_ld0
	s_cmp_lt_u32 s61, 16
	s_cbranch_scc1 .Lmy_rd1_lgo

; DI void attn_unit_a8(unsigned char* lds, const AttnArgs& a) {
;     ...
;     auto w_cvt = [&]() __attribute__((always_inline)) { unsigned char* t8 = lds + AT_WT + wn4 * WPITCH + 4 * wid;
; #pragma unroll
;         for (int j = 0; j < 4; ++j) *(unsigned*)(t8 + j * WPITCH) = pk4_fp8_mul64(wq[0][j], wq[1][j], wq[2][j], wq[3][j]); };
;     const int wcol = tid >> 1, whalf = tid & 1;
;     const unsigned wper_gu = (unsigned)((wcol >> 7) * 256 + (wcol & 96) + invperm32(wcol & 31)) * 1024u + 16u * whalf;
;     const unsigned wper_dn = (unsigned)fwd_lane16(wcol) * 1024u + 16u * whalf;
;     auto w_store = [&](int j) __attribute__((always_inline)) { const float* src; unsigned char* dst; int ld, n0, k0; bool gu; w_decode(j, src, dst, ld, n0, k0, gu);
;         const int nb = n0 >> 8; const unsigned uni = (unsigned)(gu ? (nb & 3) * 512 + (nb >> 2) * 128 : nb * 256) * 1024u + (unsigned)k0;
;         const unsigned off = (gu ? wper_gu : wper_dn) + uni;
;         const unsigned* t = (const unsigned*)(lds + AT_WT + wcol * WPITCH + 16 * whalf);
;         *(u32x4*)(dst + off) = (u32x4){t[0], t[1], t[2], t[3]}; };
;     ...
;     auto step = [&](int t, u32x2& kl, u32x2& vl, const u32x2& ks, const u32x2& vs, f32x16& c0, f32x16& c1, f32x16& n0, f32x16& n1, const int hk, const int wj) __attribute__((always_inline)) {
;         const int slot1 = slot == 2 ? 0 : slot + 1, slot2 = slot1 == 2 ? 0 : slot1 + 1;
;         if (hk == 1) { w_cvt(); w_issue(wj + 1 < AT_NWT ? wj + 1 : AT_NWT - 1); }
;         if (hk == 2) w_store(wj);
;         { const int tn = t + 3; gload(tn < a.t1 ? tn : a.t1 - 1, kl, vl); }
;         const unsigned char* Kb = lds + slot * AT_BUFB; const unsigned char* Kn = lds + slot1 * AT_BUFB;
;         const v8i k0 = kread(Kn, 0), k1 = kread(Kn, 1), v0 = vread(Kb, 0), v1 = vread(Kb, 1);
;         n0 = mfma8(k0, qf8, cinit); n1 = mfma8(k1, qf8, cinit);
;         expsum(c0); expsum(c1);
;         const v8i P = pack8(c0, c1);
;         o0[0] = mfma8(v0, P, o0[0]); o0[1] = mfma8(v1, P, o0[1]);
;         lstore(slot2, ks, vs);
;         __syncthreads();
;         slot = slot1;
;     };
;     {
;         int t = a.t0;
;         if (wrider)
;             for (int j = 0; j < AT_NWT; ++j, t += 2) { step(t, kregB, vregB, kregA, vregA, sx0, sx1, sy0, sy1, 1, j); step(t + 1, kregA, vregA, kregB, vregB, sy0, sy1, sx0, sx1, 2, j); }
.LBB0_1922:
	s_lshl_b32 s8, s18, 1
	s_waitcnt lgkmcnt(0)
	s_lshr_b32 s16, s18, 3
	s_and_b32 s8, s8, 0x600
	s_and_b32 s16, s16, 0x80
	s_or_b32 s8, s8, s16
	s_and_b64 s[14:15], s[14:15], exec
	v_pk_add_f32 v[54:55], v[164:165], v[108:109]
	s_cselect_b32 s8, s8, s18
	s_and_b32 s14, s50, 3
	v_pk_add_f32 v[54:55], v[154:155], v[54:55]
	s_add_i32 s14, s52, s14
	v_pk_add_f32 v[54:55], v[158:159], v[54:55]
	s_lshl_b32 s14, s14, 5
	s_lshl_b32 s8, s8, 10
	v_pk_add_f32 v[56:57], v[160:161], v[110:111]
	v_pk_add_f32 v[46:47], v[46:47], v[54:55]
	s_add_i32 s14, s8, s14
	s_add_i32 s51, s51, 1
	v_pk_add_f32 v[56:57], v[162:163], v[56:57]
	v_pk_add_f32 v[46:47], v[50:51], v[46:47]
	s_and_b64 s[12:13], s[12:13], exec
	v_pk_add_f32 v[56:57], v[152:153], v[56:57]
	v_pk_add_f32 v[40:41], v[40:41], v[46:47]
	s_cselect_b32 s18, 0, s51
	v_pk_add_f32 v[56:57], v[156:157], v[56:57]
	v_pk_add_f32 v[50:51], v[42:43], v[40:41]
	s_mul_i32 s8, s18, 0x4680
	v_pk_add_f32 v[44:45], v[44:45], v[56:57]
	v_add_u32_e32 v58, s8, v169
	v_pk_add_f32 v[110:111], v[34:35], v[50:51]
	v_add_u32_e32 v34, 0xd800, v175
	v_pk_add_f32 v[48:49], v[48:49], v[44:45]
	ds_read_b128 v[40:43], v58
	ds_read_b128 v[44:47], v58 offset:16
	v_add_u32_e32 v35, 0xd808, v175
	ds_read2_b32 v[54:55], v34 offset1:1
	ds_read2_b32 v[56:57], v35 offset1:1
	v_add_u32_e32 v50, v52, v170
	v_lshl_or_b32 v50, v50, 10, v172
	v_add_u32_e32 v50, s14, v50
	v_exp_f32_e32 v82, v82
	s_waitcnt lgkmcnt(0)
	global_store_dwordx4 v50, v[54:57], s[10:11]
	ds_read_b128 v[50:53], v58 offset:2560
	ds_read_b128 v[54:57], v58 offset:2576
	v_add_co_u32_e32 v58, vcc, s70, v148
	v_exp_f32_e32 v83, v83
	s_nop 0
	v_addc_co_u32_e32 v59, vcc, 0, v149, vcc
	global_load_dwordx2 v[136:137], v[58:59], off
	global_load_dwordx2 v[138:139], v[150:151], off offset:256
	v_exp_f32_e32 v86, v86
	v_exp_f32_e32 v87, v87
	v_exp_f32_e32 v90, v90
	v_exp_f32_e32 v91, v91
	v_exp_f32_e32 v94, v94
	v_exp_f32_e32 v95, v95
	v_exp_f32_e32 v164, v66
	v_exp_f32_e32 v165, v67
	v_exp_f32_e32 v178, v70
	v_exp_f32_e32 v179, v71
	v_exp_f32_e32 v74, v74
	v_exp_f32_e32 v75, v75
	v_exp_f32_e32 v78, v78
	v_exp_f32_e32 v79, v79
	ds_read_b128 v[148:151], v176 offset:5120
	ds_read_b128 v[152:155], v176 offset:5136
	ds_read_b128 v[156:159], v176 offset:7680
	ds_read_b128 v[160:163], v176 offset:7696
	v_exp_f32_e32 v84, v84
	v_exp_f32_e32 v85, v85
	v_exp_f32_e32 v88, v88
	v_exp_f32_e32 v89, v89
	v_exp_f32_e32 v92, v92
	v_exp_f32_e32 v93, v93
	v_exp_f32_e32 v96, v96
	v_exp_f32_e32 v97, v97
	v_exp_f32_e32 v176, v68
	v_exp_f32_e32 v177, v69
	v_exp_f32_e32 v180, v72
	v_exp_f32_e32 v181, v73
	v_exp_f32_e32 v76, v76
	v_exp_f32_e32 v77, v77
	v_exp_f32_e32 v80, v80
	v_exp_f32_e32 v81, v81
	s_nop 0
	s_nop 0
	s_nop 0
	s_nop 0
	s_nop 0
	s_nop 0
	s_nop 0
	s_nop 0
	v_cvt_scalef32_pk_fp8_f32 v66, v82, v83, s69
	v_cvt_scalef32_pk_fp8_f32 v70, v164, v165, s69
	v_cvt_scalef32_pk_fp8_f32 v67, v86, v87, s69
	v_cvt_scalef32_pk_fp8_f32 v71, v178, v179, s69
	v_cvt_scalef32_pk_fp8_f32 v68, v90, v91, s69
	v_cvt_scalef32_pk_fp8_f32 v72, v74, v75, s69
	v_cvt_scalef32_pk_fp8_f32 v69, v94, v95, s69
	v_cvt_scalef32_pk_fp8_f32 v73, v78, v79, s69
	v_pk_add_f32 v[36:37], v[36:37], v[48:49]
	v_cvt_scalef32_pk_fp8_f32 v66, v84, v85, s69 op_sel:[0,0,0,1]
	v_cvt_scalef32_pk_fp8_f32 v70, v176, v177, s69 op_sel:[0,0,0,1]
	v_cvt_scalef32_pk_fp8_f32 v67, v88, v89, s69 op_sel:[0,0,0,1]
	v_cvt_scalef32_pk_fp8_f32 v71, v180, v181, s69 op_sel:[0,0,0,1]
	v_cvt_scalef32_pk_fp8_f32 v68, v92, v93, s69 op_sel:[0,0,0,1]
	v_cvt_scalef32_pk_fp8_f32 v72, v76, v77, s69 op_sel:[0,0,0,1]
	v_cvt_scalef32_pk_fp8_f32 v69, v96, v97, s69 op_sel:[0,0,0,1]
	v_cvt_scalef32_pk_fp8_f32 v73, v80, v81, s69 op_sel:[0,0,0,1]
	v_pk_add_f32 v[108:109], v[38:39], v[36:37]
	v_mfma_f32_32x32x64_f8f6f4 v[34:49], v[40:47], v[98:105], 0
	v_add_f32_e64 v110, v110, v82
	v_add_f32_e64 v111, v111, v83
	v_add_f32_e64 v82, v108, v84
	v_add_f32_e64 v83, v109, v85
	v_add_f32_e64 v84, v86, v110
	v_add_f32_e64 v85, v87, v111
	v_add_f32_e64 v82, v88, v82
	v_add_f32_e64 v83, v89, v83
	s_addk_i32 s8, 0x4680
	v_add_f32_e64 v84, v90, v84
	v_add_f32_e64 v85, v91, v85
	v_add_f32_e64 v82, v92, v82
	v_add_f32_e64 v83, v93, v83
	s_cmp_lg_u32 s18, 2
	v_pk_add_f32 v[82:83], v[96:97], v[82:83]
	v_pk_add_f32 v[84:85], v[94:95], v[84:85]
	s_cselect_b32 s8, s8, 0
	v_pk_add_f32 v[84:85], v[164:165], v[84:85]
	v_pk_add_f32 v[82:83], v[176:177], v[82:83]
	s_add_i32 s8, s8, 0
	v_pk_add_f32 v[82:83], v[180:181], v[82:83]
	s_waitcnt lgkmcnt(4)
	v_mfma_f32_32x32x64_f8f6f4 v[50:65], v[50:57], v[98:105], 0
	v_add_f32_e64 v84, v178, v84
	v_add_f32_e64 v85, v179, v85
	v_add_f32_e64 v76, v76, v82
	v_add_f32_e64 v77, v77, v83
	v_add_f32_e64 v74, v74, v84
	v_add_f32_e64 v75, v75, v85
	s_add_i32 s50, s50, 1
	s_addk_i32 s23, 0x80
	v_add_f32_e64 v110, v80, v76
	v_add_f32_e64 v111, v81, v77
	v_add_f32_e64 v108, v78, v74
	v_add_f32_e64 v109, v79, v75
	v_lshl_add_u64 v[140:141], v[140:141], 0, s[36:37]
	s_cmp_lg_u32 s50, 8
	v_lshl_add_u64 v[142:143], v[142:143], 0, s[38:39]
	s_waitcnt lgkmcnt(2)
	v_mfma_f32_32x32x64_f8f6f4 v[18:33], v[148:155], v[66:73], v[18:33]
	s_waitcnt lgkmcnt(0)
	v_mfma_f32_32x32x64_f8f6f4 v[2:17], v[156:163], v[66:73], v[2:17]
	v_add_u32_e32 v66, s8, v131
	s_waitcnt vmcnt(4)
	ds_write_b64 v66, v[144:145]
	v_add_u32_e32 v66, s8, v168
	v_add_u32_e32 v66, 0x1400, v66
	s_waitcnt vmcnt(3)
	ds_write2_b32 v66, v146, v147 offset1:8
	s_waitcnt lgkmcnt(0)
	s_barrier
	s_cbranch_scc0 .LBB0_1931
.LBB0_1923:
	s_min_u32 s19, s50, 6
	s_add_i32 s19, s19, 1
	s_lshl_b32 s8, s19, 7
	s_and_b32 s8, s8, 0x1e00
	s_nop 0
	s_nop 0
	s_add_i32 s10, s8, s76
	v_cvt_scalef32_pk_fp8_f32 v66, v116, v112, s66
	v_cvt_scalef32_pk_fp8_f32 v67, v117, v113, s66
	s_mul_hi_u32 s8, s10, 0xaaaaaaab
	v_cvt_scalef32_pk_fp8_f32 v66, v120, v124, s66 op_sel:[0,0,0,1]
	v_cvt_scalef32_pk_fp8_f32 v67, v121, v125, s66 op_sel:[0,0,0,1]
	v_add_u32_e32 v68, 0xd800, v174
	s_lshr_b32 s8, s8, 6
	ds_write2_b32 v68, v66, v67 offset1:9
	s_nop 0
	s_nop 0
	s_mul_i32 s52, s8, 0xffffffa0
	v_cvt_scalef32_pk_fp8_f32 v66, v118, v114, s66
	v_cvt_scalef32_pk_fp8_f32 v67, v119, v115, s66
	s_add_i32 s52, s52, s10
	v_cvt_scalef32_pk_fp8_f32 v66, v122, v126, s66 op_sel:[0,0,0,1]
	v_cvt_scalef32_pk_fp8_f32 v67, v123, v127, s66 op_sel:[0,0,0,1]
	s_mov_b64 s[14:15], s[0:1]
	s_cmp_gt_i32 s52, 63
	s_mov_b64 s[16:17], -1
	ds_write2_b32 v68, v66, v67 offset0:18 offset1:27
	s_cbranch_scc0 .LBB0_1925
	s_load_dwordx2 s[10:11], s[14:15], 0xc0
	s_lshl_b64 s[12:13], s[8:9], 22
	s_mov_b64 s[16:17], 0
	s_waitcnt lgkmcnt(0)
	s_add_u32 s10, s10, s12
	s_addc_u32 s11, s11, s13
	s_add_u32 s10, s10, 0x8000000
	s_addc_u32 s11, s11, 0
	s_and_b32 s12, s52, 0x7ffffffc
	s_sub_i32 s51, s12, 64
